# nt hint on the 179 streaming f32 source loads of the prologue phase (weights, p, x are read exactly once), on top of the previous stack
# speedup vs baseline: 1.0067x; 1.0018x over previous
.LBB0_47:
	s_andn2_b64 vcc, exec, s[8:9]
	s_cbranch_vccnz .LBB0_97
	s_lshl_b32 s8, s4, 6
	s_add_i32 s46, s8, 0xff9cc000
	v_or_b32_e32 v2, s46, v57
	v_lshlrev_b32_e32 v58, 4, v2
	v_lshl_add_u64 v[82:83], v[58:59], 2, v[70:71]
	v_mov_b32_e32 v2, 0
	v_mov_b32_e32 v6, 0
	v_mov_b32_e32 v7, 0
	v_mov_b32_e32 v8, 0
	v_mov_b32_e32 v9, 0
	s_and_saveexec_b64 s[8:9], s[6:7]
	s_cbranch_execz .LBB0_50
	global_load_dwordx4 v[6:9], v[82:83], off nt
.LBB0_50:
	s_or_b64 exec, exec, s[8:9]
	v_mov_b32_e32 v3, 0
	v_mov_b32_e32 v4, 0
	v_mov_b32_e32 v5, 0
	s_and_saveexec_b64 s[8:9], s[6:7]
	s_cbranch_execz .LBB0_52
	global_load_dwordx4 v[2:5], v[82:83], off offset:512 nt
.LBB0_52:
	s_or_b64 exec, exec, s[8:9]
	v_mov_b32_e32 v10, 0
	v_mov_b32_e32 v14, 0
	v_mov_b32_e32 v15, 0
	v_mov_b32_e32 v16, 0
	v_mov_b32_e32 v17, 0
	s_and_saveexec_b64 s[8:9], s[6:7]
	s_cbranch_execz .LBB0_54
	global_load_dwordx4 v[14:17], v[82:83], off offset:1024 nt
.LBB0_54:
	s_or_b64 exec, exec, s[8:9]
	v_mov_b32_e32 v11, 0
	v_mov_b32_e32 v12, 0
	v_mov_b32_e32 v13, 0
	s_and_saveexec_b64 s[8:9], s[6:7]
	s_cbranch_execz .LBB0_56
	global_load_dwordx4 v[10:13], v[82:83], off offset:1536 nt
.LBB0_56:
	s_or_b64 exec, exec, s[8:9]
	v_mov_b32_e32 v18, 0
	v_mov_b32_e32 v22, 0
	v_mov_b32_e32 v23, 0
	v_mov_b32_e32 v24, 0
	v_mov_b32_e32 v25, 0
	s_and_saveexec_b64 s[8:9], s[6:7]
	s_cbranch_execz .LBB0_58
	global_load_dwordx4 v[22:25], v[82:83], off offset:2048 nt
.LBB0_58:
	s_or_b64 exec, exec, s[8:9]
	v_mov_b32_e32 v19, 0
	v_mov_b32_e32 v20, 0
	v_mov_b32_e32 v21, 0
	s_and_saveexec_b64 s[8:9], s[6:7]
	s_cbranch_execz .LBB0_60
	global_load_dwordx4 v[18:21], v[82:83], off offset:2560 nt
.LBB0_60:
	s_or_b64 exec, exec, s[8:9]
	v_mov_b32_e32 v26, 0
	v_mov_b32_e32 v30, 0
	v_mov_b32_e32 v31, 0
	v_mov_b32_e32 v32, 0
	v_mov_b32_e32 v33, 0
	s_and_saveexec_b64 s[8:9], s[6:7]
	s_cbranch_execz .LBB0_62
	global_load_dwordx4 v[30:33], v[82:83], off offset:3072 nt
.LBB0_62:
	s_or_b64 exec, exec, s[8:9]
	v_mov_b32_e32 v27, 0
	v_mov_b32_e32 v28, 0
	v_mov_b32_e32 v29, 0
	s_and_saveexec_b64 s[8:9], s[6:7]
	s_cbranch_execz .LBB0_64
	global_load_dwordx4 v[26:29], v[82:83], off offset:3584 nt

.LBB0_98:
	s_andn2_b64 vcc, exec, s[8:9]
	s_cbranch_vccnz .LBB0_135
	s_add_i32 s46, s4, 0xfffe7b00
	s_lshr_b32 s58, s46, 9
	s_cmp_eq_u32 s58, 2
	s_cselect_b32 s8, 10, 14
	s_cmp_lg_u32 s58, 1
	s_waitcnt lgkmcnt(0)
	s_cselect_b32 s50, s8, 9
	s_cmpk_lt_u32 s46, 0x200
	s_cselect_b64 s[8:9], -1, 0
	s_and_b64 s[48:49], s[8:9], exec
	s_cselect_b32 s48, 13, s50
	s_lshl_b32 s48, s48, 3
	s_load_dwordx2 s[50:51], s[90:91], s48 offset:0x0
	s_lshl_b32 s46, s46, 1
	s_and_b32 s48, s46, 0x3c0
	s_lshl_b32 s46, s4, 5
	s_and_b32 s75, s46, 0x3e0
	v_or_b32_e32 v2, s48, v57
	s_cmp_lg_u32 s58, 3
	s_mov_b64 s[60:61], -1
	v_lshlrev_b32_e32 v58, 12, v2
	s_cbranch_scc0 .LBB0_133
	s_and_b64 s[8:9], s[8:9], exec
	s_cselect_b32 s61, s54, s39
	s_cselect_b32 s60, s33, s38
	s_waitcnt lgkmcnt(0)
	v_lshl_add_u64 v[2:3], s[50:51], 0, v[58:59]
	s_lshl_b32 s46, s75, 2
	v_lshl_add_u64 v[2:3], v[2:3], 0, s[46:47]
	v_lshlrev_b32_e32 v4, 2, v60
	v_mov_b32_e32 v5, v59
	v_lshl_add_u64 v[30:31], v[2:3], 0, v[4:5]
	v_add_co_u32_e32 v6, vcc, s64, v30
	v_add_u32_e32 v75, 0x420, v87
	s_nop 0
	v_addc_co_u32_e32 v7, vcc, 0, v31, vcc
	v_add_co_u32_e32 v10, vcc, s65, v30
	global_load_dwordx4 v[2:5], v[30:31], off nt
	s_nop 0
	global_load_dwordx4 v[6:9], v[6:7], off nt
	v_addc_co_u32_e32 v11, vcc, 0, v31, vcc
	v_add_co_u32_e32 v14, vcc, s66, v30
	v_add_u32_e32 v77, 0x428, v87
	s_nop 0
	v_addc_co_u32_e32 v15, vcc, 0, v31, vcc
	v_add_co_u32_e32 v18, vcc, s67, v30
	global_load_dwordx4 v[10:13], v[10:11], off nt
	s_nop 0
	global_load_dwordx4 v[14:17], v[14:15], off nt
	v_addc_co_u32_e32 v19, vcc, 0, v31, vcc
	v_add_co_u32_e32 v22, vcc, s68, v30
	v_add_u32_e32 v79, 0x840, v87
	s_nop 0
	v_addc_co_u32_e32 v23, vcc, 0, v31, vcc
	global_load_dwordx4 v[18:21], v[18:19], off nt
	s_nop 0
	global_load_dwordx4 v[22:25], v[22:23], off nt
	v_add_co_u32_e32 v26, vcc, s69, v30
	v_add_u32_e32 v81, 0x848, v87
	s_nop 0
	v_addc_co_u32_e32 v27, vcc, 0, v31, vcc
	global_load_dwordx4 v[26:29], v[26:27], off nt
	v_add_co_u32_e32 v30, vcc, s70, v30
	v_add_u32_e32 v82, 0xc60, v87
	s_nop 0
	v_addc_co_u32_e32 v31, vcc, 0, v31, vcc
	global_load_dwordx4 v[30:33], v[30:31], off nt
	v_add_u32_e32 v83, 0xc68, v87
	v_add_u32_e32 v93, 0x1080, v87
	v_add_u32_e32 v94, 0x1088, v87
	v_add_u32_e32 v95, 0x14a0, v87
	v_add_u32_e32 v96, 0x14a8, v87
	v_add_u32_e32 v97, 0x18c0, v87
	v_add_u32_e32 v98, 0x18c8, v87
	v_add_u32_e32 v99, 0x1ce0, v87
	v_add_u32_e32 v100, 0x1ce8, v87
	s_cmp_lg_u64 s[60:61], 0
	s_cselect_b64 s[62:63], -1, 0
	s_cmp_eq_u64 s[60:61], 0
	s_waitcnt vmcnt(7)
	ds_write2_b32 v87, v2, v3 offset1:1
	ds_write2_b32 v87, v4, v5 offset0:2 offset1:3
	s_waitcnt vmcnt(6)
	ds_write2_b32 v75, v6, v7 offset1:1
	ds_write2_b32 v77, v8, v9 offset1:1
	s_waitcnt vmcnt(5)
	ds_write2_b32 v79, v10, v11 offset1:1
	ds_write2_b32 v81, v12, v13 offset1:1
	s_waitcnt vmcnt(4)
	ds_write2_b32 v82, v14, v15 offset1:1
	ds_write2_b32 v83, v16, v17 offset1:1
	s_waitcnt vmcnt(3)
	ds_write2_b32 v93, v18, v19 offset1:1
	ds_write2_b32 v94, v20, v21 offset1:1
	s_waitcnt vmcnt(2)
	ds_write2_b32 v95, v22, v23 offset1:1
	ds_write2_b32 v96, v24, v25 offset1:1
	s_waitcnt vmcnt(1)
	ds_write2_b32 v97, v26, v27 offset1:1
	ds_write2_b32 v98, v28, v29 offset1:1
	s_waitcnt vmcnt(0)
	ds_write2_b32 v99, v30, v31 offset1:1
	ds_write2_b32 v100, v32, v33 offset1:1
	s_waitcnt lgkmcnt(0)
	v_or_b32_e32 v3, s48, v62
	v_mov_b32_e32 v2, 0x41800000
	v_lshlrev_b32_e32 v14, 2, v3
	v_mov_b32_e32 v3, 0x41800000
	s_cbranch_scc1 .LBB0_102
	global_load_dword v3, v14, s[60:61]
	s_waitcnt vmcnt(0)
	v_mul_f32_e32 v3, 0x41800000, v3

.LBB0_133:
	s_and_b64 vcc, exec, s[60:61]
	s_cbranch_vccz .LBB0_135
	s_waitcnt lgkmcnt(0)
	v_lshl_add_u64 v[2:3], s[50:51], 0, v[58:59]
	s_lshl_b32 s46, s75, 2
	v_lshl_add_u64 v[2:3], v[2:3], 0, s[46:47]
	v_lshlrev_b32_e32 v58, 2, v60
	v_lshl_add_u64 v[30:31], v[2:3], 0, v[58:59]
	v_add_co_u32_e32 v6, vcc, 0x8000, v30
	v_add_u32_e32 v58, 0x420, v87
	s_nop 0
	v_addc_co_u32_e32 v7, vcc, 0, v31, vcc
	v_add_co_u32_e32 v10, vcc, 0x10000, v30
	global_load_dwordx4 v[2:5], v[30:31], off nt
	s_nop 0
	global_load_dwordx4 v[6:9], v[6:7], off nt
	v_addc_co_u32_e32 v11, vcc, 0, v31, vcc
	v_add_co_u32_e32 v14, vcc, 0x18000, v30
	v_add_u32_e32 v75, 0x428, v87
	s_nop 0
	v_addc_co_u32_e32 v15, vcc, 0, v31, vcc
	v_add_co_u32_e32 v18, vcc, 0x20000, v30
	global_load_dwordx4 v[10:13], v[10:11], off nt
	s_nop 0
	global_load_dwordx4 v[14:17], v[14:15], off nt
	v_addc_co_u32_e32 v19, vcc, 0, v31, vcc
	v_add_co_u32_e32 v22, vcc, 0x28000, v30
	v_add_u32_e32 v77, 0x840, v87
	s_nop 0
	v_addc_co_u32_e32 v23, vcc, 0, v31, vcc
	global_load_dwordx4 v[18:21], v[18:19], off nt
	s_nop 0
	global_load_dwordx4 v[22:25], v[22:23], off nt
	v_add_co_u32_e32 v26, vcc, 0x30000, v30
	v_add_u32_e32 v79, 0x848, v87
	s_nop 0
	v_addc_co_u32_e32 v27, vcc, 0, v31, vcc
	global_load_dwordx4 v[26:29], v[26:27], off nt
	v_add_co_u32_e32 v30, vcc, 0x38000, v30
	v_add_u32_e32 v81, 0xc60, v87
	s_nop 0
	v_addc_co_u32_e32 v31, vcc, 0, v31, vcc
	global_load_dwordx4 v[30:33], v[30:31], off nt
	v_add_u32_e32 v93, 0xc68, v87
	v_add_u32_e32 v96, 0x1080, v87
	v_add_u32_e32 v97, 0x1088, v87
	v_add_u32_e32 v98, 0x14a0, v87
	v_add_u32_e32 v99, 0x14a8, v87
	v_add_u32_e32 v100, 0x18c0, v87
	v_add_u32_e32 v101, 0x18c8, v87
	v_add_u32_e32 v102, 0x1ce0, v87
	v_add_u32_e32 v103, 0x1ce8, v87
	v_add_u32_e32 v104, 0x400, v89
	v_mov_b32_e32 v94, v59
	v_mov_b32_e32 v95, v59
	s_mov_b32 s49, s47
	v_lshl_add_u64 v[82:83], v[72:73], 0, s[48:49]
	s_waitcnt vmcnt(7)
	ds_write2_b32 v87, v2, v3 offset1:1
	ds_write2_b32 v87, v4, v5 offset0:2 offset1:3
	s_waitcnt vmcnt(6)
	ds_write2_b32 v58, v6, v7 offset1:1
	ds_write2_b32 v75, v8, v9 offset1:1
	s_waitcnt vmcnt(5)
	ds_write2_b32 v77, v10, v11 offset1:1
	ds_write2_b32 v79, v12, v13 offset1:1
	s_waitcnt vmcnt(4)
	ds_write2_b32 v81, v14, v15 offset1:1
	ds_write2_b32 v93, v16, v17 offset1:1
	s_waitcnt vmcnt(3)
	ds_write2_b32 v96, v18, v19 offset1:1
	ds_write2_b32 v97, v20, v21 offset1:1
	s_waitcnt vmcnt(2)
	ds_write2_b32 v98, v22, v23 offset1:1
	ds_write2_b32 v99, v24, v25 offset1:1
	s_waitcnt vmcnt(1)
	ds_write2_b32 v100, v26, v27 offset1:1
	ds_write2_b32 v101, v28, v29 offset1:1
	s_waitcnt vmcnt(0)
	ds_write2_b32 v102, v30, v31 offset1:1
	ds_write2_b32 v103, v32, v33 offset1:1
	s_waitcnt lgkmcnt(0)
	ds_read2_b32 v[2:3], v89 offset1:16
	ds_read2_b32 v[4:5], v89 offset0:33 offset1:49
	ds_read2_b32 v[6:7], v89 offset0:66 offset1:82
	ds_read2_b32 v[8:9], v89 offset0:99 offset1:115
	ds_read2_b32 v[10:11], v89 offset0:132 offset1:148
	ds_read2_b32 v[12:13], v89 offset0:165 offset1:181
	ds_read2_b32 v[14:15], v89 offset0:198 offset1:214
	ds_read2_b32 v[16:17], v89 offset0:231 offset1:247
	ds_read2_b32 v[18:19], v104 offset0:8 offset1:24
	ds_read2_b32 v[20:21], v104 offset0:41 offset1:57
	s_waitcnt lgkmcnt(9)
	v_mul_f32_e32 v2, 0x41800000, v2
	s_waitcnt lgkmcnt(8)
	v_mul_f32_e32 v4, 0x41800000, v4
	s_waitcnt lgkmcnt(5)
	v_mul_f32_e32 v10, 0x41800000, v10
	v_cvt_pk_fp8_f32 v94, v2, v4
	s_waitcnt lgkmcnt(4)
	v_mul_f32_e32 v2, 0x41800000, v12
	v_cvt_pk_fp8_f32 v95, v10, v2
	ds_read2_b32 v[22:23], v104 offset0:74 offset1:90
	ds_read2_b32 v[24:25], v104 offset0:107 offset1:123
	ds_read2_b32 v[26:27], v104 offset0:140 offset1:156
	ds_read2_b32 v[28:29], v104 offset0:173 offset1:189
	s_waitcnt lgkmcnt(7)
	v_mul_f32_e32 v2, 0x41800000, v14
	s_waitcnt lgkmcnt(6)
	v_mul_f32_e32 v4, 0x41800000, v16
	v_mul_f32_e32 v6, 0x41800000, v6
	v_mul_f32_e32 v8, 0x41800000, v8
	v_cvt_pk_fp8_f32 v95, v2, v4 op_sel:[0,0,1]
	s_waitcnt lgkmcnt(5)
	v_mul_f32_e32 v2, 0x41800000, v18
	s_waitcnt lgkmcnt(4)
	v_mul_f32_e32 v4, 0x41800000, v20
	v_mov_b32_e32 v96, v59
	ds_read2_b32 v[30:31], v104 offset0:206 offset1:222
	ds_read2_b32 v[32:33], v104 offset0:239 offset1:255
	v_cvt_pk_fp8_f32 v94, v6, v8 op_sel:[0,0,1]
	v_cvt_pk_fp8_f32 v96, v2, v4
	s_waitcnt lgkmcnt(3)
	v_mul_f32_e32 v6, 0x41800000, v26
	s_waitcnt lgkmcnt(2)
	v_mul_f32_e32 v8, 0x41800000, v28
	v_mov_b32_e32 v97, v59
	v_cvt_pk_fp8_f32 v97, v6, v8
	v_mul_f32_e32 v2, 0x41800000, v22
	v_mul_f32_e32 v4, 0x41800000, v24
	v_cvt_pk_fp8_f32 v96, v2, v4 op_sel:[0,0,1]
	s_waitcnt lgkmcnt(1)
	v_mul_f32_e32 v2, 0x41800000, v30
	s_waitcnt lgkmcnt(0)
	v_mul_f32_e32 v4, 0x41800000, v32
	v_cvt_pk_fp8_f32 v97, v2, v4 op_sel:[0,0,1]
	v_or_b32_e32 v2, s75, v88
	v_lshlrev_b32_e32 v58, 10, v2
	v_mul_f32_e32 v3, 0x41800000, v3
	v_mul_f32_e32 v4, 0x41800000, v5
	v_mov_b32_e32 v2, v59
	v_cvt_pk_fp8_f32 v2, v3, v4
	v_mul_f32_e32 v4, 0x41800000, v7
	v_mul_f32_e32 v6, 0x41800000, v11
	v_mul_f32_e32 v7, 0x41800000, v13
	v_mov_b32_e32 v3, v59
	v_cvt_pk_fp8_f32 v3, v6, v7
	v_mul_f32_e32 v5, 0x41800000, v9
	v_cvt_pk_fp8_f32 v2, v4, v5 op_sel:[0,0,1]
	v_mul_f32_e32 v4, 0x41800000, v15
	v_mul_f32_e32 v5, 0x41800000, v17
	v_cvt_pk_fp8_f32 v3, v4, v5 op_sel:[0,0,1]
	v_mul_f32_e32 v5, 0x41800000, v19
	v_mul_f32_e32 v6, 0x41800000, v21
	v_mov_b32_e32 v4, v59
	v_cvt_pk_fp8_f32 v4, v5, v6
	v_mul_f32_e32 v8, 0x41800000, v27
	v_mul_f32_e32 v9, 0x41800000, v29
	v_mov_b32_e32 v5, v59
	v_cvt_pk_fp8_f32 v5, v8, v9
	v_mul_f32_e32 v6, 0x41800000, v23
	v_mul_f32_e32 v7, 0x41800000, v25
	v_cvt_pk_fp8_f32 v4, v6, v7 op_sel:[0,0,1]
	v_mul_f32_e32 v6, 0x41800000, v31
	v_mul_f32_e32 v7, 0x41800000, v33
	v_cvt_pk_fp8_f32 v5, v6, v7 op_sel:[0,0,1]
	v_or_b32_e32 v6, s75, v90
	v_lshl_add_u64 v[98:99], v[82:83], 0, v[58:59]
	v_lshlrev_b32_e32 v58, 10, v6
	v_lshl_add_u64 v[6:7], v[82:83], 0, v[58:59]
	global_store_dwordx4 v[98:99], v[94:97], off
	global_store_dwordx4 v[6:7], v[2:5], off
	s_waitcnt lgkmcnt(0)

.LBB0_141:
	s_andn2_b64 vcc, exec, s[8:9]
	s_cbranch_vccnz .LBB0_175
	s_add_i32 s8, s4, 0xfffe8000
	s_lshr_b32 s46, s8, 9
	s_lshl_b64 s[8:9], s[46:47], 22
	s_add_u32 s8, s28, s8
	s_addc_u32 s9, s29, s9
	s_lshl_b32 s48, s4, 1
	s_and_b32 s48, s48, 0x3c0
	s_lshl_b32 s49, s4, 5
	s_waitcnt lgkmcnt(0)
	s_lshl_b32 s50, s46, 10
	s_mov_b32 s51, s47
	s_and_b32 s58, s49, 0x3e0
	s_lshl_b64 s[50:51], s[50:51], 2
	v_or_b32_e32 v2, s48, v57
	s_add_u32 s50, s10, s50
	v_lshlrev_b32_e32 v58, 12, v2
	s_addc_u32 s51, s11, s51
	v_lshl_add_u64 v[2:3], s[8:9], 0, v[58:59]
	s_lshl_b32 s8, s58, 2
	s_mov_b32 s9, s47
	v_lshl_add_u64 v[2:3], v[2:3], 0, s[8:9]
	v_lshlrev_b32_e32 v58, 2, v60
	v_lshl_add_u64 v[2:3], v[2:3], 0, v[58:59]
	v_add_co_u32_e32 v8, vcc, s64, v2
	v_add_u32_e32 v32, 0x428, v87
	s_nop 0
	v_addc_co_u32_e32 v9, vcc, 0, v3, vcc
	v_add_co_u32_e32 v12, vcc, s65, v2
	global_load_dwordx4 v[4:7], v[2:3], off nt
	s_nop 0
	global_load_dwordx4 v[8:11], v[8:9], off nt
	v_addc_co_u32_e32 v13, vcc, 0, v3, vcc
	v_add_co_u32_e32 v16, vcc, s66, v2
	v_add_u32_e32 v33, 0x840, v87
	s_nop 0
	v_addc_co_u32_e32 v17, vcc, 0, v3, vcc
	v_add_co_u32_e32 v20, vcc, s67, v2
	global_load_dwordx4 v[12:15], v[12:13], off nt
	s_nop 0
	global_load_dwordx4 v[16:19], v[16:17], off nt
	v_addc_co_u32_e32 v21, vcc, 0, v3, vcc
	v_add_co_u32_e32 v24, vcc, s68, v2
	v_add_u32_e32 v58, 0x848, v87
	s_nop 0
	v_addc_co_u32_e32 v25, vcc, 0, v3, vcc
	global_load_dwordx4 v[20:23], v[20:21], off nt
	s_nop 0
	global_load_dwordx4 v[24:27], v[24:25], off nt
	v_add_co_u32_e32 v28, vcc, s69, v2
	v_add_u32_e32 v75, 0xc60, v87
	s_nop 0
	v_addc_co_u32_e32 v29, vcc, 0, v3, vcc
	global_load_dwordx4 v[28:31], v[28:29], off nt
	v_add_co_u32_e32 v2, vcc, s70, v2
	v_add_u32_e32 v77, 0xc68, v87
	s_nop 0
	v_addc_co_u32_e32 v3, vcc, 0, v3, vcc
	global_load_dwordx4 v[94:97], v[2:3], off nt
	v_add_u32_e32 v3, 0x420, v87
	v_add_u32_e32 v79, 0x1080, v87
	v_add_u32_e32 v81, 0x1088, v87
	v_add_u32_e32 v82, 0x14a0, v87
	v_add_u32_e32 v83, 0x14a8, v87
	v_add_u32_e32 v93, 0x18c0, v87
	v_add_u32_e32 v98, 0x18c8, v87
	v_add_u32_e32 v99, 0x1ce0, v87
	v_add_u32_e32 v100, 0x1ce8, v87
	v_cndmask_b32_e64 v101, 0, 1, s[44:45]
	v_or_b32_e32 v102, s48, v62
	v_mov_b32_e32 v2, 0x41800000
	v_cmp_ne_u32_e64 s[8:9], 1, v101
	s_andn2_b64 vcc, exec, s[44:45]
	s_waitcnt vmcnt(7)
	ds_write2_b32 v87, v4, v5 offset1:1
	ds_write2_b32 v87, v6, v7 offset0:2 offset1:3
	s_waitcnt vmcnt(6)
	ds_write2_b32 v3, v8, v9 offset1:1
	ds_write2_b32 v32, v10, v11 offset1:1
	s_waitcnt vmcnt(5)
	ds_write2_b32 v33, v12, v13 offset1:1
	ds_write2_b32 v58, v14, v15 offset1:1
	s_waitcnt vmcnt(4)
	ds_write2_b32 v75, v16, v17 offset1:1
	ds_write2_b32 v77, v18, v19 offset1:1
	s_waitcnt vmcnt(3)
	ds_write2_b32 v79, v20, v21 offset1:1
	ds_write2_b32 v81, v22, v23 offset1:1
	s_waitcnt vmcnt(2)
	ds_write2_b32 v82, v24, v25 offset1:1
	ds_write2_b32 v83, v26, v27 offset1:1
	s_waitcnt vmcnt(1)
	ds_write2_b32 v93, v28, v29 offset1:1
	ds_write2_b32 v98, v30, v31 offset1:1
	s_waitcnt vmcnt(0)
	ds_write2_b32 v99, v94, v95 offset1:1
	ds_write2_b32 v100, v96, v97 offset1:1
	s_waitcnt lgkmcnt(0)
	v_lshlrev_b32_e32 v14, 2, v102
	v_mov_b32_e32 v3, 0x41800000
	s_cbranch_vccnz .LBB0_144
	global_load_dword v3, v14, s[50:51]
	s_waitcnt vmcnt(0)
	v_mul_f32_e32 v3, 0x41800000, v3

.LBB0_176:
	s_andn2_b64 vcc, exec, s[8:9]
	s_cbranch_vccnz .LBB0_178
	s_add_i32 s8, s4, 0xffff0000
	s_lshr_b32 s46, s8, 9
	s_lshl_b64 s[8:9], s[46:47], 20
	s_lshl_b64 s[48:49], s[46:47], 22
	s_add_u32 s58, s24, s48
	s_addc_u32 s59, s25, s49
	s_lshl_b32 s46, s4, 1
	s_and_b32 s48, s46, 0x3c0
	s_lshl_b32 s46, s4, 5
	v_or_b32_e32 v2, s48, v57
	s_waitcnt lgkmcnt(0)
	s_and_b32 s50, s46, 0x3e0
	v_lshlrev_b32_e32 v58, 12, v2
	v_lshl_add_u64 v[2:3], s[58:59], 0, v[58:59]
	s_lshl_b32 s46, s50, 2
	v_lshl_add_u64 v[2:3], v[2:3], 0, s[46:47]
	v_lshlrev_b32_e32 v58, 2, v60
	v_lshl_add_u64 v[30:31], v[2:3], 0, v[58:59]
	v_add_co_u32_e32 v6, vcc, s64, v30
	v_add_u32_e32 v58, 0x420, v87
	s_nop 0
	v_addc_co_u32_e32 v7, vcc, 0, v31, vcc
	v_add_co_u32_e32 v10, vcc, s65, v30
	global_load_dwordx4 v[2:5], v[30:31], off nt
	s_nop 0
	global_load_dwordx4 v[6:9], v[6:7], off nt
	v_addc_co_u32_e32 v11, vcc, 0, v31, vcc
	v_add_co_u32_e32 v14, vcc, s66, v30
	v_add_u32_e32 v75, 0x428, v87
	s_nop 0
	v_addc_co_u32_e32 v15, vcc, 0, v31, vcc
	v_add_co_u32_e32 v18, vcc, s67, v30
	global_load_dwordx4 v[10:13], v[10:11], off nt
	s_nop 0
	global_load_dwordx4 v[14:17], v[14:15], off nt
	v_addc_co_u32_e32 v19, vcc, 0, v31, vcc
	v_add_co_u32_e32 v22, vcc, s68, v30
	v_add_u32_e32 v77, 0x840, v87
	s_nop 0
	v_addc_co_u32_e32 v23, vcc, 0, v31, vcc
	global_load_dwordx4 v[18:21], v[18:19], off nt
	s_nop 0
	global_load_dwordx4 v[22:25], v[22:23], off nt
	v_add_co_u32_e32 v26, vcc, s69, v30
	v_add_u32_e32 v79, 0x848, v87
	s_nop 0
	v_addc_co_u32_e32 v27, vcc, 0, v31, vcc
	global_load_dwordx4 v[26:29], v[26:27], off nt
	v_add_co_u32_e32 v30, vcc, s70, v30
	v_add_u32_e32 v81, 0xc60, v87
	s_nop 0
	v_addc_co_u32_e32 v31, vcc, 0, v31, vcc
	global_load_dwordx4 v[30:33], v[30:31], off nt
	v_add_u32_e32 v93, 0xc68, v87
	v_add_u32_e32 v96, 0x1080, v87
	v_add_u32_e32 v97, 0x1088, v87
	v_add_u32_e32 v98, 0x14a0, v87
	v_add_u32_e32 v99, 0x14a8, v87
	v_add_u32_e32 v100, 0x18c0, v87
	v_add_u32_e32 v101, 0x18c8, v87
	v_add_u32_e32 v102, 0x1ce0, v87
	v_add_u32_e32 v103, 0x1ce8, v87
	v_mov_b32_e32 v94, v59
	v_mov_b32_e32 v95, v59
	s_mov_b32 s49, s47
	v_lshl_add_u64 v[82:83], v[46:47], 0, s[8:9]
	v_lshl_add_u64 v[82:83], v[82:83], 0, s[48:49]
	v_lshl_add_u64 v[82:83], v[82:83], 0, v[62:63]
	s_waitcnt vmcnt(7)
	ds_write2_b32 v87, v2, v3 offset1:1
	ds_write2_b32 v87, v4, v5 offset0:2 offset1:3
	s_waitcnt vmcnt(6)
	ds_write2_b32 v58, v6, v7 offset1:1
	ds_write2_b32 v75, v8, v9 offset1:1
	s_waitcnt vmcnt(5)
	ds_write2_b32 v77, v10, v11 offset1:1
	ds_write2_b32 v79, v12, v13 offset1:1
	s_waitcnt vmcnt(4)
	ds_write2_b32 v81, v14, v15 offset1:1
	ds_write2_b32 v93, v16, v17 offset1:1
	s_waitcnt vmcnt(3)
	ds_write2_b32 v96, v18, v19 offset1:1
	ds_write2_b32 v97, v20, v21 offset1:1
	s_waitcnt vmcnt(2)
	ds_write2_b32 v98, v22, v23 offset1:1
	ds_write2_b32 v99, v24, v25 offset1:1
	s_waitcnt vmcnt(1)
	ds_write2_b32 v100, v26, v27 offset1:1
	ds_write2_b32 v101, v28, v29 offset1:1
	s_waitcnt vmcnt(0)
	ds_write2_b32 v102, v30, v31 offset1:1
	ds_write2_b32 v103, v32, v33 offset1:1
	s_waitcnt lgkmcnt(0)
	ds_read2_b32 v[2:3], v89 offset1:16
	ds_read2_b32 v[4:5], v89 offset0:33 offset1:49
	ds_read2_b32 v[6:7], v89 offset0:66 offset1:82
	ds_read2_b32 v[8:9], v89 offset0:99 offset1:115
	ds_read2_b32 v[10:11], v89 offset0:132 offset1:148
	ds_read2_b32 v[12:13], v89 offset0:165 offset1:181
	s_waitcnt lgkmcnt(5)
	v_mul_f32_e32 v2, 0x41800000, v2
	s_waitcnt lgkmcnt(4)
	v_mul_f32_e32 v4, 0x41800000, v4
	v_cvt_pk_fp8_f32 v94, v2, v4
	s_waitcnt lgkmcnt(1)
	v_mul_f32_e32 v2, 0x41800000, v10
	s_waitcnt lgkmcnt(0)
	v_mul_f32_e32 v4, 0x41800000, v12
	v_cvt_pk_fp8_f32 v95, v2, v4
	ds_read2_b32 v[14:15], v89 offset0:198 offset1:214
	ds_read2_b32 v[16:17], v89 offset0:231 offset1:247
	v_add_u32_e32 v2, 0x400, v89
	ds_read2_b32 v[18:19], v2 offset0:8 offset1:24
	ds_read2_b32 v[20:21], v2 offset0:41 offset1:57
	ds_read2_b32 v[22:23], v2 offset0:74 offset1:90
	ds_read2_b32 v[24:25], v2 offset0:107 offset1:123
	ds_read2_b32 v[26:27], v2 offset0:140 offset1:156
	ds_read2_b32 v[28:29], v2 offset0:173 offset1:189
	v_mul_f32_e32 v6, 0x41800000, v6
	v_mul_f32_e32 v8, 0x41800000, v8
	v_cvt_pk_fp8_f32 v94, v6, v8 op_sel:[0,0,1]
	s_waitcnt lgkmcnt(7)
	v_mul_f32_e32 v4, 0x41800000, v14
	s_waitcnt lgkmcnt(6)
	v_mul_f32_e32 v6, 0x41800000, v16
	v_cvt_pk_fp8_f32 v95, v4, v6 op_sel:[0,0,1]
	s_waitcnt lgkmcnt(5)
	v_mul_f32_e32 v4, 0x41800000, v18
	s_waitcnt lgkmcnt(4)
	v_mul_f32_e32 v6, 0x41800000, v20
	v_mov_b32_e32 v96, v59
	ds_read2_b32 v[30:31], v2 offset0:206 offset1:222
	ds_read2_b32 v[32:33], v2 offset0:239 offset1:255
	v_cvt_pk_fp8_f32 v96, v4, v6
	s_waitcnt lgkmcnt(3)
	v_mul_f32_e32 v8, 0x41800000, v26
	s_waitcnt lgkmcnt(2)
	v_mul_f32_e32 v10, 0x41800000, v28
	v_mov_b32_e32 v97, v59
	v_cvt_pk_fp8_f32 v97, v8, v10
	v_mul_f32_e32 v4, 0x41800000, v22
	v_mul_f32_e32 v6, 0x41800000, v24
	v_cvt_pk_fp8_f32 v96, v4, v6 op_sel:[0,0,1]
	s_waitcnt lgkmcnt(1)
	v_mul_f32_e32 v2, 0x41800000, v30
	s_waitcnt lgkmcnt(0)
	v_mul_f32_e32 v4, 0x41800000, v32
	v_cvt_pk_fp8_f32 v97, v2, v4 op_sel:[0,0,1]
	v_or_b32_e32 v2, s50, v88
	v_lshlrev_b32_e32 v58, 10, v2
	v_mul_f32_e32 v3, 0x41800000, v3
	v_mul_f32_e32 v4, 0x41800000, v5
	v_mov_b32_e32 v2, v59
	v_cvt_pk_fp8_f32 v2, v3, v4
	v_mul_f32_e32 v4, 0x41800000, v7
	v_mul_f32_e32 v6, 0x41800000, v11
	v_mul_f32_e32 v7, 0x41800000, v13
	v_mov_b32_e32 v3, v59
	v_cvt_pk_fp8_f32 v3, v6, v7
	v_mul_f32_e32 v5, 0x41800000, v9
	v_cvt_pk_fp8_f32 v2, v4, v5 op_sel:[0,0,1]
	v_mul_f32_e32 v4, 0x41800000, v15
	v_mul_f32_e32 v5, 0x41800000, v17
	v_cvt_pk_fp8_f32 v3, v4, v5 op_sel:[0,0,1]
	v_mul_f32_e32 v5, 0x41800000, v19
	v_mul_f32_e32 v6, 0x41800000, v21
	v_mov_b32_e32 v4, v59
	v_cvt_pk_fp8_f32 v4, v5, v6
	v_mul_f32_e32 v8, 0x41800000, v27
	v_mul_f32_e32 v9, 0x41800000, v29
	v_mov_b32_e32 v5, v59
	v_cvt_pk_fp8_f32 v5, v8, v9
	v_mul_f32_e32 v6, 0x41800000, v23
	v_mul_f32_e32 v7, 0x41800000, v25
	v_cvt_pk_fp8_f32 v4, v6, v7 op_sel:[0,0,1]
	v_mul_f32_e32 v6, 0x41800000, v31
	v_mul_f32_e32 v7, 0x41800000, v33
	v_cvt_pk_fp8_f32 v5, v6, v7 op_sel:[0,0,1]
	v_or_b32_e32 v6, s50, v90
	v_lshl_add_u64 v[98:99], v[82:83], 0, v[58:59]
	v_lshlrev_b32_e32 v58, 10, v6
	v_lshl_add_u64 v[6:7], v[82:83], 0, v[58:59]
	global_store_dwordx4 v[98:99], v[94:97], off
	global_store_dwordx4 v[6:7], v[2:5], off
	s_waitcnt lgkmcnt(0)

.LBB0_180:
	s_waitcnt lgkmcnt(0)
	s_ashr_i32 s50, s4, 10
	s_lshl_b32 s8, s4, 5
	s_ashr_i32 s51, s50, 31
	s_and_b32 s48, s4, 0x3c0
	s_and_b32 s49, s8, 0x7e0
	s_lshl_b64 s[8:9], s[50:51], 23
	s_add_u32 s8, s20, s8
	s_addc_u32 s9, s21, s9
	s_ashr_i32 s46, s4, 5
	s_and_b32 s58, s46, 0xfffffc00
	s_ashr_i32 s59, s58, 31
	s_lshl_b64 s[58:59], s[58:59], 2
	v_or_b32_e32 v2, s48, v57
	s_add_u32 s58, s18, s58
	v_lshlrev_b32_e32 v58, 13, v2
	s_addc_u32 s59, s19, s59
	v_lshl_add_u64 v[2:3], s[8:9], 0, v[58:59]
	s_lshl_b32 s46, s49, 2
	v_lshl_add_u64 v[2:3], v[2:3], 0, s[46:47]
	v_lshlrev_b32_e32 v58, 2, v60
	v_lshl_add_u64 v[2:3], v[2:3], 0, v[58:59]
	v_add_co_u32_e32 v8, vcc, s65, v2
	v_add_u32_e32 v32, 0x428, v87
	s_nop 0
	v_addc_co_u32_e32 v9, vcc, 0, v3, vcc
	v_add_co_u32_e32 v12, vcc, s67, v2
	global_load_dwordx4 v[4:7], v[2:3], off nt
	s_nop 0
	global_load_dwordx4 v[8:11], v[8:9], off nt
	v_addc_co_u32_e32 v13, vcc, 0, v3, vcc
	v_add_co_u32_e32 v16, vcc, s69, v2
	v_add_u32_e32 v33, 0x840, v87
	s_nop 0
	v_addc_co_u32_e32 v17, vcc, 0, v3, vcc
	v_add_co_u32_e32 v20, vcc, s71, v2
	global_load_dwordx4 v[12:15], v[12:13], off nt
	s_nop 0
	global_load_dwordx4 v[16:19], v[16:17], off nt
	v_addc_co_u32_e32 v21, vcc, 0, v3, vcc
	v_add_co_u32_e32 v24, vcc, s72, v2
	v_add_u32_e32 v58, 0x848, v87
	s_nop 0
	v_addc_co_u32_e32 v25, vcc, 0, v3, vcc
	global_load_dwordx4 v[20:23], v[20:21], off nt
	s_nop 0
	global_load_dwordx4 v[24:27], v[24:25], off nt
	v_add_co_u32_e32 v28, vcc, s73, v2
	v_add_u32_e32 v75, 0xc60, v87
	s_nop 0
	v_addc_co_u32_e32 v29, vcc, 0, v3, vcc
	global_load_dwordx4 v[28:31], v[28:29], off nt
	v_add_co_u32_e32 v2, vcc, s74, v2
	v_add_u32_e32 v77, 0xc68, v87
	s_nop 0
	v_addc_co_u32_e32 v3, vcc, 0, v3, vcc
	global_load_dwordx4 v[94:97], v[2:3], off nt
	v_add_u32_e32 v3, 0x420, v87
	v_add_u32_e32 v79, 0x1080, v87
	v_add_u32_e32 v81, 0x1088, v87
	v_add_u32_e32 v82, 0x14a0, v87
	v_add_u32_e32 v83, 0x14a8, v87
	v_add_u32_e32 v93, 0x18c0, v87
	v_add_u32_e32 v98, 0x18c8, v87
	v_add_u32_e32 v99, 0x1ce0, v87
	v_add_u32_e32 v100, 0x1ce8, v87
	v_cndmask_b32_e64 v101, 0, 1, s[40:41]
	v_or_b32_e32 v102, s48, v62
	v_mov_b32_e32 v2, 1.0
	v_cmp_ne_u32_e64 s[8:9], 1, v101
	s_andn2_b64 vcc, exec, s[40:41]
	s_waitcnt vmcnt(7)
	ds_write2_b32 v87, v4, v5 offset1:1
	ds_write2_b32 v87, v6, v7 offset0:2 offset1:3
	s_waitcnt vmcnt(6)
	ds_write2_b32 v3, v8, v9 offset1:1
	ds_write2_b32 v32, v10, v11 offset1:1
	s_waitcnt vmcnt(5)
	ds_write2_b32 v33, v12, v13 offset1:1
	ds_write2_b32 v58, v14, v15 offset1:1
	s_waitcnt vmcnt(4)
	ds_write2_b32 v75, v16, v17 offset1:1
	ds_write2_b32 v77, v18, v19 offset1:1
	s_waitcnt vmcnt(3)
	ds_write2_b32 v79, v20, v21 offset1:1
	ds_write2_b32 v81, v22, v23 offset1:1
	s_waitcnt vmcnt(2)
	ds_write2_b32 v82, v24, v25 offset1:1
	ds_write2_b32 v83, v26, v27 offset1:1
	s_waitcnt vmcnt(1)
	ds_write2_b32 v93, v28, v29 offset1:1
	ds_write2_b32 v98, v30, v31 offset1:1
	s_waitcnt vmcnt(0)
	ds_write2_b32 v99, v94, v95 offset1:1
	ds_write2_b32 v100, v96, v97 offset1:1
	s_waitcnt lgkmcnt(0)
	v_lshlrev_b32_e32 v6, 2, v102
	v_mov_b32_e32 v3, 1.0
	s_cbranch_vccnz .LBB0_182
	global_load_dword v3, v6, s[58:59]

.LBB0_244:
	global_load_dwordx4 v[8:11], v[2:3], off offset:-16 nt
	global_load_dwordx4 v[12:15], v[2:3], off nt
	v_lshl_add_u64 v[6:7], v[6:7], 0, s[10:11]
	v_cmp_lt_u64_e32 vcc, s[20:21], v[6:7]
	v_lshl_add_u64 v[2:3], v[2:3], 0, s[8:9]
	s_or_b64 s[18:19], vcc, s[18:19]
	s_waitcnt vmcnt(1)
	v_bfe_u32 v1, v8, 16, 1
	v_bfe_u32 v16, v9, 16, 1
	v_bfe_u32 v17, v10, 16, 1
	v_bfe_u32 v18, v11, 16, 1
	s_waitcnt vmcnt(0)
	v_bfe_u32 v19, v12, 16, 1
	v_bfe_u32 v20, v13, 16, 1
	v_bfe_u32 v21, v14, 16, 1
	v_bfe_u32 v22, v15, 16, 1
	v_add3_u32 v1, v8, v1, s1
	v_add3_u32 v8, v9, v16, s1
	v_add3_u32 v9, v10, v17, s1
	v_add3_u32 v10, v11, v18, s1
	v_add3_u32 v11, v12, v19, s1
	v_add3_u32 v12, v13, v20, s1
	v_add3_u32 v13, v14, v21, s1
	v_add3_u32 v14, v15, v22, s1
	v_lshrrev_b32_e32 v1, 16, v1
	v_lshrrev_b32_e32 v9, 16, v9
	v_lshrrev_b32_e32 v11, 16, v11
	v_lshrrev_b32_e32 v13, 16, v13
	v_and_or_b32 v8, v8, s4, v1
	v_and_or_b32 v9, v10, s4, v9
	v_and_or_b32 v10, v12, s4, v11
	v_and_or_b32 v11, v14, s4, v13
	global_store_dwordx4 v[4:5], v[8:11], off
	v_lshl_add_u64 v[4:5], v[4:5], 0, s[14:15]
	s_andn2_b64 exec, exec, s[18:19]
	s_cbranch_execnz .LBB0_244
.LBB0_245:
	s_or_b64 exec, exec, s[6:7]
	v_and_b32_e32 v6, 0xff, v53
	s_cmpk_gt_i32 s2, 0x1ff
	v_readfirstlane_b32 s1, v6
	v_mbcnt_lo_u32_b32 v202, -1, 0
	s_waitcnt lgkmcnt(0)
	s_barrier
	s_cbranch_scc1 .LBB0_429
	v_lshlrev_b32_e32 v8, 4, v6
	global_load_dwordx4 v[2:5], v8, s[16:17] nt
	v_mov_b32_e32 v9, 0
	s_bfe_u32 s15, s0, 0x20006
	s_lshr_b32 s22, s1, 6
	v_ashrrev_i32_e32 v7, 2, v53
	v_lshl_add_u64 v[166:167], s[12:13], 0, v[8:9]
	v_lshlrev_b32_e32 v8, 3, v6
	v_and_b32_e32 v179, 0xffffffc0, v7
	s_cmp_gt_u32 s1, 63
	v_lshl_add_u64 v[6:7], v[34:35], 0, v[8:9]
	s_mov_b64 s[0:1], 0x4fc00000
	v_lshl_add_u64 v[168:169], v[6:7], 0, s[0:1]
	v_mbcnt_hi_u32_b32 v6, -1, v202
	v_and_b32_e32 v7, 64, v6
	v_add_u32_e32 v7, 64, v7
	v_xor_b32_e32 v8, 1, v6
	v_cmp_lt_i32_e32 vcc, v8, v7
	v_and_b32_e32 v1, 0xffffff00, v53
	v_add_u32_e32 v1, 0, v1
	v_cndmask_b32_e32 v8, v6, v8, vcc
	v_lshlrev_b32_e32 v180, 2, v8
	v_xor_b32_e32 v8, 2, v6
	v_cmp_lt_i32_e32 vcc, v8, v7
	s_mov_b32 s23, 0
	v_lshl_add_u32 v178, s15, 2, v1
	v_cndmask_b32_e32 v8, v6, v8, vcc
	v_lshlrev_b32_e32 v181, 2, v8
	v_xor_b32_e32 v8, 4, v6
	v_cmp_lt_i32_e32 vcc, v8, v7
	s_cselect_b64 s[10:11], -1, 0
	v_cmp_eq_u32_e64 s[6:7], 0, v55
	v_cndmask_b32_e32 v8, v6, v8, vcc
	v_lshlrev_b32_e32 v182, 2, v8
	v_xor_b32_e32 v8, 8, v6
	v_cmp_lt_i32_e32 vcc, v8, v7
	v_lshl_add_u32 v186, s2, 7, v179
	s_lshl_b32 s13, s3, 7
	v_cndmask_b32_e32 v8, v6, v8, vcc
	v_lshlrev_b32_e32 v183, 2, v8
	v_xor_b32_e32 v8, 16, v6
	v_cmp_lt_i32_e32 vcc, v8, v7
	s_mov_b32 s24, 0xffff0000
	v_mov_b32_e32 v187, 0x358637bd
	v_cndmask_b32_e32 v8, v6, v8, vcc
	v_lshlrev_b32_e32 v184, 2, v8
	v_xor_b32_e32 v8, 32, v6
	v_cmp_lt_i32_e32 vcc, v8, v7
	s_movk_i32 s25, 0x7fff
	s_mov_b32 s12, 0x3e000000
	v_cndmask_b32_e32 v6, v6, v8, vcc
	v_lshlrev_b32_e32 v185, 2, v6
	s_mov_b32 s14, 0x3e800000
	s_mov_b32 s26, s2
	s_branch .LBB0_248

.LBB0_248:
	v_lshl_add_u32 v170, s26, 7, v179
	v_and_b32_e32 v188, 0x1fc0, v170
	v_cmp_ne_u32_e64 s[8:9], 0, v188
	s_mov_b64 s[16:17], -1
	s_and_b64 vcc, exec, s[10:11]
	s_cbranch_vccz .LBB0_385
	v_and_b32_e32 v189, 0x1fc0, v186
	s_mov_b64 s[20:21], -1
	s_mov_b64 s[16:17], 0
	s_cmp_lt_i32 s22, 2
	s_mov_b64 s[18:19], 0
	s_cbranch_scc1 .LBB0_339
	s_cmp_eq_u32 s22, 2
	s_mov_b64 s[18:19], -1
	s_cbranch_scc0 .LBB0_294
	v_mov_b32_e32 v6, 0
	s_waitcnt vmcnt(14)
	v_mov_b32_e32 v10, 0
	v_mov_b32_e32 v11, 0
	v_mov_b32_e32 v12, 0
	v_mov_b32_e32 v13, 0
	s_and_saveexec_b64 s[18:19], s[8:9]
	s_cbranch_execz .LBB0_253
	v_ashrrev_i32_e32 v171, 31, v170
	v_lshlrev_b64 v[8:9], 12, v[170:171]
	v_lshl_add_u64 v[8:9], v[166:167], 0, v[8:9]
	v_add_co_u32_e32 v8, vcc, 0xffff0000, v8
	s_nop 1
	v_addc_co_u32_e32 v9, vcc, -1, v9, vcc
	global_load_dwordx4 v[10:13], v[8:9], off nt
.LBB0_253:
	s_or_b64 exec, exec, s[18:19]
	v_mov_b32_e32 v7, 0
	v_mov_b32_e32 v8, 0
	v_mov_b32_e32 v9, 0
	s_and_saveexec_b64 s[18:19], s[8:9]
	s_cbranch_execz .LBB0_255
	v_ashrrev_i32_e32 v171, 31, v170
	v_lshlrev_b64 v[6:7], 12, v[170:171]
	v_lshl_add_u64 v[6:7], v[166:167], 0, v[6:7]
	v_add_co_u32_e32 v6, vcc, 0xffff1000, v6
	s_nop 1
	v_addc_co_u32_e32 v7, vcc, -1, v7, vcc
	global_load_dwordx4 v[6:9], v[6:7], off nt
.LBB0_255:
	s_or_b64 exec, exec, s[18:19]
	v_mov_b32_e32 v14, 0
	s_waitcnt vmcnt(12)
	v_mov_b32_e32 v22, 0
	v_mov_b32_e32 v23, 0
	v_mov_b32_e32 v24, 0
	v_mov_b32_e32 v25, 0
	s_and_saveexec_b64 s[18:19], s[8:9]
	s_cbranch_execz .LBB0_257
	v_ashrrev_i32_e32 v171, 31, v170
	v_lshlrev_b64 v[16:17], 12, v[170:171]
	v_lshl_add_u64 v[16:17], v[166:167], 0, v[16:17]
	v_add_co_u32_e32 v16, vcc, 0xffff2000, v16
	s_nop 1
	v_addc_co_u32_e32 v17, vcc, -1, v17, vcc
	global_load_dwordx4 v[22:25], v[16:17], off nt
.LBB0_257:
	s_or_b64 exec, exec, s[18:19]
	v_mov_b32_e32 v15, 0
	v_mov_b32_e32 v16, 0
	v_mov_b32_e32 v17, 0
	s_and_saveexec_b64 s[18:19], s[8:9]
	s_cbranch_execz .LBB0_259
	v_ashrrev_i32_e32 v171, 31, v170
	v_lshlrev_b64 v[14:15], 12, v[170:171]
	v_lshl_add_u64 v[14:15], v[166:167], 0, v[14:15]
	v_add_co_u32_e32 v14, vcc, 0xffff3000, v14
	s_nop 1
	v_addc_co_u32_e32 v15, vcc, -1, v15, vcc
	global_load_dwordx4 v[14:17], v[14:15], off nt
.LBB0_259:
	s_or_b64 exec, exec, s[18:19]
	v_mov_b32_e32 v18, 0
	s_waitcnt vmcnt(10)
	v_mov_b32_e32 v30, 0
	v_mov_b32_e32 v31, 0
	v_mov_b32_e32 v32, 0
	v_mov_b32_e32 v33, 0
	s_and_saveexec_b64 s[18:19], s[8:9]
	s_cbranch_execz .LBB0_261
	v_ashrrev_i32_e32 v171, 31, v170
	v_lshlrev_b64 v[20:21], 12, v[170:171]
	v_lshl_add_u64 v[20:21], v[166:167], 0, v[20:21]
	v_add_co_u32_e32 v20, vcc, 0xffff4000, v20
	s_nop 1
	v_addc_co_u32_e32 v21, vcc, -1, v21, vcc
	global_load_dwordx4 v[30:33], v[20:21], off nt
.LBB0_261:
	s_or_b64 exec, exec, s[18:19]
	v_mov_b32_e32 v19, 0
	v_mov_b32_e32 v20, 0
	v_mov_b32_e32 v21, 0
	s_and_saveexec_b64 s[18:19], s[8:9]
	s_cbranch_execz .LBB0_263
	v_ashrrev_i32_e32 v171, 31, v170
	v_lshlrev_b64 v[18:19], 12, v[170:171]
	v_lshl_add_u64 v[18:19], v[166:167], 0, v[18:19]
	v_add_co_u32_e32 v18, vcc, 0xffff5000, v18
	s_nop 1
	v_addc_co_u32_e32 v19, vcc, -1, v19, vcc
	global_load_dwordx4 v[18:21], v[18:19], off nt
.LBB0_263:
	s_or_b64 exec, exec, s[18:19]
	v_mov_b32_e32 v26, 0
	v_mov_b32_e32 v34, 0
	v_mov_b32_e32 v35, 0
	v_mov_b32_e32 v36, 0
	v_mov_b32_e32 v37, 0
	s_and_saveexec_b64 s[18:19], s[8:9]
	s_cbranch_execz .LBB0_265
	v_ashrrev_i32_e32 v171, 31, v170
	v_lshlrev_b64 v[28:29], 12, v[170:171]
	v_lshl_add_u64 v[28:29], v[166:167], 0, v[28:29]
	v_add_co_u32_e32 v28, vcc, 0xffff6000, v28
	s_nop 1
	v_addc_co_u32_e32 v29, vcc, -1, v29, vcc
	global_load_dwordx4 v[34:37], v[28:29], off nt
.LBB0_265:
	s_or_b64 exec, exec, s[18:19]
	v_mov_b32_e32 v27, 0
	v_mov_b32_e32 v28, 0
	v_mov_b32_e32 v29, 0
	s_and_saveexec_b64 s[18:19], s[8:9]
	s_cbranch_execz .LBB0_267
	v_ashrrev_i32_e32 v171, 31, v170
	v_lshlrev_b64 v[26:27], 12, v[170:171]
	v_lshl_add_u64 v[26:27], v[166:167], 0, v[26:27]
	v_add_co_u32_e32 v26, vcc, 0xffff7000, v26
	s_nop 1
	v_addc_co_u32_e32 v27, vcc, -1, v27, vcc
	global_load_dwordx4 v[26:29], v[26:27], off nt

.LBB0_269:
	s_or_b64 exec, exec, s[18:19]
	v_mov_b32_e32 v10, 0
	v_mov_b32_e32 v14, 0
	s_waitcnt lgkmcnt(3)
	v_mov_b32_e32 v15, 0
	v_mov_b32_e32 v16, 0
	s_waitcnt lgkmcnt(2)
	v_mov_b32_e32 v17, 0
	s_waitcnt lgkmcnt(0)
	s_barrier
	s_and_saveexec_b64 s[18:19], s[8:9]
	s_cbranch_execz .LBB0_271
	v_ashrrev_i32_e32 v171, 31, v170
	v_lshlrev_b64 v[6:7], 12, v[170:171]
	v_lshl_add_u64 v[6:7], v[166:167], 0, v[6:7]
	v_add_co_u32_e32 v6, vcc, 0xffff8000, v6
	s_nop 1
	v_addc_co_u32_e32 v7, vcc, -1, v7, vcc
	global_load_dwordx4 v[14:17], v[6:7], off nt
.LBB0_271:
	s_or_b64 exec, exec, s[18:19]
	v_mov_b32_e32 v11, 0
	v_mov_b32_e32 v12, 0
	v_mov_b32_e32 v13, 0
	s_and_saveexec_b64 s[18:19], s[8:9]
	s_cbranch_execz .LBB0_273
	v_ashrrev_i32_e32 v171, 31, v170
	v_lshlrev_b64 v[6:7], 12, v[170:171]
	v_lshl_add_u64 v[6:7], v[166:167], 0, v[6:7]
	v_add_co_u32_e32 v6, vcc, 0xffff9000, v6
	s_nop 1
	v_addc_co_u32_e32 v7, vcc, -1, v7, vcc
	global_load_dwordx4 v[10:13], v[6:7], off nt
.LBB0_273:
	s_or_b64 exec, exec, s[18:19]
	v_mov_b32_e32 v22, 0
	v_mov_b32_e32 v26, 0
	v_mov_b32_e32 v27, 0
	v_mov_b32_e32 v28, 0
	v_mov_b32_e32 v29, 0
	s_and_saveexec_b64 s[18:19], s[8:9]
	s_cbranch_execz .LBB0_275
	v_ashrrev_i32_e32 v171, 31, v170
	v_lshlrev_b64 v[6:7], 12, v[170:171]
	v_lshl_add_u64 v[6:7], v[166:167], 0, v[6:7]
	v_add_co_u32_e32 v6, vcc, 0xffffa000, v6
	s_nop 1
	v_addc_co_u32_e32 v7, vcc, -1, v7, vcc
	global_load_dwordx4 v[26:29], v[6:7], off nt
.LBB0_275:
	s_or_b64 exec, exec, s[18:19]
	v_mov_b32_e32 v23, 0
	v_mov_b32_e32 v24, 0
	v_mov_b32_e32 v25, 0
	s_and_saveexec_b64 s[18:19], s[8:9]
	s_cbranch_execz .LBB0_277
	v_ashrrev_i32_e32 v171, 31, v170
	v_lshlrev_b64 v[6:7], 12, v[170:171]
	v_lshl_add_u64 v[6:7], v[166:167], 0, v[6:7]
	v_add_co_u32_e32 v6, vcc, 0xffffb000, v6
	s_nop 1
	v_addc_co_u32_e32 v7, vcc, -1, v7, vcc
	global_load_dwordx4 v[22:25], v[6:7], off nt
.LBB0_277:
	s_or_b64 exec, exec, s[18:19]
	v_mov_b32_e32 v30, 0
	v_mov_b32_e32 v34, 0
	v_mov_b32_e32 v35, 0
	v_mov_b32_e32 v36, 0
	v_mov_b32_e32 v37, 0
	s_and_saveexec_b64 s[18:19], s[8:9]
	s_cbranch_execz .LBB0_279
	v_ashrrev_i32_e32 v171, 31, v170
	v_lshlrev_b64 v[6:7], 12, v[170:171]
	v_lshl_add_u64 v[6:7], v[166:167], 0, v[6:7]
	v_add_co_u32_e32 v6, vcc, 0xffffc000, v6
	s_nop 1
	v_addc_co_u32_e32 v7, vcc, -1, v7, vcc
	global_load_dwordx4 v[34:37], v[6:7], off nt
.LBB0_279:
	s_or_b64 exec, exec, s[18:19]
	v_mov_b32_e32 v31, 0
	v_mov_b32_e32 v32, 0
	v_mov_b32_e32 v33, 0
	s_and_saveexec_b64 s[18:19], s[8:9]
	s_cbranch_execz .LBB0_281
	v_ashrrev_i32_e32 v171, 31, v170
	v_lshlrev_b64 v[6:7], 12, v[170:171]
	v_lshl_add_u64 v[6:7], v[166:167], 0, v[6:7]
	v_add_co_u32_e32 v6, vcc, 0xffffd000, v6
	s_nop 1
	v_addc_co_u32_e32 v7, vcc, -1, v7, vcc
	global_load_dwordx4 v[30:33], v[6:7], off nt
.LBB0_281:
	s_or_b64 exec, exec, s[18:19]
	v_mov_b32_e32 v38, 0
	v_mov_b32_e32 v42, 0
	v_mov_b32_e32 v43, 0
	v_mov_b32_e32 v44, 0
	v_mov_b32_e32 v45, 0
	s_and_saveexec_b64 s[18:19], s[8:9]
	s_cbranch_execz .LBB0_283
	v_ashrrev_i32_e32 v171, 31, v170
	v_lshlrev_b64 v[6:7], 12, v[170:171]
	v_lshl_add_u64 v[6:7], v[166:167], 0, v[6:7]
	v_add_co_u32_e32 v6, vcc, 0xffffe000, v6
	s_nop 1
	v_addc_co_u32_e32 v7, vcc, -1, v7, vcc
	global_load_dwordx4 v[42:45], v[6:7], off nt
.LBB0_283:
	s_or_b64 exec, exec, s[18:19]
	v_mov_b32_e32 v39, 0
	v_mov_b32_e32 v40, 0
	v_mov_b32_e32 v41, 0
	s_and_saveexec_b64 s[18:19], s[8:9]
	s_cbranch_execz .LBB0_285
	v_ashrrev_i32_e32 v171, 31, v170
	v_lshlrev_b64 v[6:7], 12, v[170:171]
	v_lshl_add_u64 v[6:7], v[166:167], 0, v[6:7]
	global_load_dwordx4 v[38:41], v[6:7], off offset:-4096 nt

.LBB0_287:
	s_or_b64 exec, exec, s[18:19]
	s_waitcnt lgkmcnt(0)
	s_barrier
	ds_read_b128 v[6:9], v47
	ds_read_b128 v[18:21], v47 offset:16
	ds_read_b128 v[50:53], v47 offset:32
	ds_read_b128 v[54:57], v47 offset:48
	v_ashrrev_i32_e32 v171, 31, v170
	s_waitcnt lgkmcnt(3)
	v_mov_b32_e32 v48, v7
	v_mov_b32_e32 v49, v8
	v_mov_b32_e32 v7, v9
	v_pk_add_f32 v[6:7], v[48:49], v[6:7]
	s_mov_b32 s1, 0
	v_add_f32_e32 v6, v6, v7
	v_fmamk_f32 v6, v6, 0x3a800000, v187
	v_rsq_f32_e32 v46, v6
	s_waitcnt lgkmcnt(2)
	v_mov_b32_e32 v6, v19
	v_mov_b32_e32 v7, v20
	v_mov_b32_e32 v19, v21
	v_pk_add_f32 v[6:7], v[6:7], v[18:19]
	ds_read_b128 v[66:69], v47 offset:80
	v_add_f32_e32 v6, v6, v7
	v_fmamk_f32 v6, v6, 0x3a800000, v187
	v_rsq_f32_e32 v48, v6
	s_waitcnt lgkmcnt(2)
	v_mov_b32_e32 v6, v51
	v_mov_b32_e32 v7, v52
	v_mov_b32_e32 v51, v53
	v_pk_add_f32 v[6:7], v[6:7], v[50:51]
	s_mov_b32 s0, s23
	v_add_f32_e32 v6, v6, v7
	v_fmamk_f32 v6, v6, 0x3a800000, v187
	v_rsq_f32_e32 v50, v6
	s_waitcnt lgkmcnt(1)
	v_mov_b32_e32 v6, v55
	v_mov_b32_e32 v7, v56
	v_mov_b32_e32 v55, v57
	v_pk_add_f32 v[18:19], v[6:7], v[54:55]
	ds_read_b128 v[6:9], v47 offset:64
	v_add_f32_e32 v18, v18, v19
	v_fmamk_f32 v18, v18, 0x3a800000, v187
	v_rsq_f32_e32 v52, v18
	v_pk_mul_f32 v[26:27], v[26:27], v[50:51] op_sel_hi:[1,0]
	s_waitcnt lgkmcnt(0)
	v_mov_b32_e32 v18, v7
	v_mov_b32_e32 v19, v8
	v_mov_b32_e32 v7, v9
	v_pk_add_f32 v[6:7], v[18:19], v[6:7]
	v_pk_mul_f32 v[28:29], v[28:29], v[50:51] op_sel_hi:[1,0]
	v_add_f32_e32 v6, v6, v7
	v_fmamk_f32 v6, v6, 0x3a800000, v187
	v_rsq_f32_e32 v58, v6
	v_lshlrev_b64 v[6:7], 12, v[170:171]
	v_lshl_add_u64 v[60:61], v[166:167], 0, v[6:7]
	v_or_b32_e32 v6, 1, v170
	v_ashrrev_i32_e32 v7, 31, v6
	v_lshlrev_b64 v[6:7], 12, v[6:7]
	v_lshl_add_u64 v[74:75], v[166:167], 0, v[6:7]
	v_or_b32_e32 v6, 2, v170
	v_ashrrev_i32_e32 v7, 31, v6
	v_lshlrev_b64 v[6:7], 12, v[6:7]
	v_lshl_add_u64 v[76:77], v[166:167], 0, v[6:7]
	v_or_b32_e32 v6, 3, v170
	v_ashrrev_i32_e32 v7, 31, v6
	v_lshlrev_b64 v[6:7], 12, v[6:7]
	v_lshl_add_u64 v[82:83], v[166:167], 0, v[6:7]
	v_or_b32_e32 v6, 4, v170
	v_ashrrev_i32_e32 v7, 31, v6
	v_lshlrev_b64 v[6:7], 12, v[6:7]
	v_lshl_add_u64 v[84:85], v[166:167], 0, v[6:7]
	v_or_b32_e32 v6, 5, v170
	v_ashrrev_i32_e32 v7, 31, v6
	v_lshlrev_b64 v[6:7], 12, v[6:7]
	v_lshl_add_u64 v[90:91], v[166:167], 0, v[6:7]
	v_or_b32_e32 v6, 6, v170
	v_ashrrev_i32_e32 v7, 31, v6
	v_lshlrev_b64 v[6:7], 12, v[6:7]
	v_lshl_add_u64 v[92:93], v[166:167], 0, v[6:7]
	v_or_b32_e32 v6, 7, v170
	v_ashrrev_i32_e32 v7, 31, v6
	v_lshlrev_b64 v[6:7], 12, v[6:7]
	v_lshl_add_u64 v[98:99], v[166:167], 0, v[6:7]
	global_load_dwordx4 v[18:21], v[92:93], off nt
	global_load_dwordx4 v[6:9], v[98:99], off nt
	global_load_dwordx4 v[62:65], v[84:85], off nt
	global_load_dwordx4 v[54:57], v[90:91], off nt
	global_load_dwordx4 v[78:81], v[76:77], off nt
	global_load_dwordx4 v[70:73], v[82:83], off nt
	global_load_dwordx4 v[94:97], v[60:61], off nt
	global_load_dwordx4 v[86:89], v[74:75], off nt
	v_mov_b32_e32 v60, v67
	v_mov_b32_e32 v61, v68
	v_mov_b32_e32 v67, v69
	v_pk_add_f32 v[60:61], v[60:61], v[66:67]
	ds_read_b128 v[66:69], v47 offset:96
	ds_read_b128 v[74:77], v47 offset:112
	v_add_f32_e32 v49, v60, v61
	v_fmamk_f32 v49, v49, 0x3a800000, v187
	v_rsq_f32_e32 v60, v49
	s_waitcnt lgkmcnt(1)
	v_mov_b32_e32 v82, v67
	v_mov_b32_e32 v83, v68
	v_mov_b32_e32 v67, v69
	v_pk_add_f32 v[66:67], v[82:83], v[66:67]
	v_pk_mul_f32 v[10:11], v[10:11], v[48:49] op_sel_hi:[1,0]
	v_add_f32_e32 v47, v66, v67
	s_waitcnt lgkmcnt(0)
	v_mov_b32_e32 v66, v75
	v_mov_b32_e32 v67, v76
	v_mov_b32_e32 v75, v77
	v_fmamk_f32 v47, v47, 0x3a800000, v187
	v_pk_add_f32 v[66:67], v[66:67], v[74:75]
	v_rsq_f32_e32 v102, v47
	v_add_f32_e32 v47, v66, v67
	v_fmamk_f32 v47, v47, 0x3a800000, v187
	v_pk_mul_f32 v[14:15], v[14:15], v[46:47] op_sel_hi:[1,0]
	v_pk_mul_f32 v[16:17], v[16:17], v[46:47] op_sel_hi:[1,0]
	v_pk_mul_f32 v[98:99], v[2:3], v[14:15]
	v_pk_mul_f32 v[100:101], v[4:5], v[16:17]
	v_pk_mul_f32 v[12:13], v[12:13], v[48:49] op_sel_hi:[1,0]
	v_pk_fma_f32 v[14:15], v[2:3], v[14:15], 0 op_sel_hi:[1,1,0]
	v_pk_fma_f32 v[16:17], v[4:5], v[16:17], 0 op_sel_hi:[1,1,0]
	v_pk_mul_f32 v[92:93], v[4:5], v[12:13]
	v_pk_mul_f32 v[90:91], v[2:3], v[10:11]
	v_pk_fma_f32 v[12:13], v[4:5], v[12:13], v[16:17]
	v_pk_fma_f32 v[10:11], v[2:3], v[10:11], v[14:15]
	v_rsq_f32_e32 v104, v47
	v_pk_mul_f32 v[46:47], v[22:23], v[52:53] op_sel_hi:[1,0]
	v_pk_mul_f32 v[48:49], v[24:25], v[52:53] op_sel_hi:[1,0]
	v_pk_fma_f32 v[10:11], v[2:3], v[26:27], v[10:11]
	v_pk_fma_f32 v[12:13], v[4:5], v[28:29], v[12:13]
	v_pk_mul_f32 v[34:35], v[34:35], v[58:59] op_sel_hi:[1,0]
	v_pk_mul_f32 v[36:37], v[36:37], v[58:59] op_sel_hi:[1,0]
	v_pk_fma_f32 v[12:13], v[4:5], v[48:49], v[12:13]
	v_pk_fma_f32 v[10:11], v[2:3], v[46:47], v[10:11]
	v_pk_mul_f32 v[30:31], v[30:31], v[60:61] op_sel_hi:[1,0]
	v_pk_mul_f32 v[32:33], v[32:33], v[60:61] op_sel_hi:[1,0]
	v_pk_fma_f32 v[10:11], v[2:3], v[34:35], v[10:11]
	v_pk_fma_f32 v[12:13], v[4:5], v[36:37], v[12:13]
	v_pk_mul_f32 v[42:43], v[42:43], v[102:103] op_sel_hi:[1,0]
	v_pk_mul_f32 v[44:45], v[44:45], v[102:103] op_sel_hi:[1,0]
	v_pk_fma_f32 v[12:13], v[4:5], v[32:33], v[12:13]
	v_pk_fma_f32 v[10:11], v[2:3], v[30:31], v[10:11]
	v_pk_mul_f32 v[38:39], v[38:39], v[104:105] op_sel_hi:[1,0]
	v_pk_mul_f32 v[40:41], v[40:41], v[104:105] op_sel_hi:[1,0]
	v_pk_fma_f32 v[10:11], v[2:3], v[42:43], v[10:11]
	v_pk_fma_f32 v[12:13], v[4:5], v[44:45], v[12:13]
	v_pk_mul_f32 v[84:85], v[4:5], v[28:29]
	v_pk_mul_f32 v[82:83], v[2:3], v[26:27]
	v_pk_mul_f32 v[76:77], v[4:5], v[48:49]
	v_pk_mul_f32 v[74:75], v[2:3], v[46:47]
	v_pk_mul_f32 v[68:69], v[4:5], v[36:37]
	v_pk_mul_f32 v[66:67], v[2:3], v[34:35]
	v_pk_mul_f32 v[60:61], v[4:5], v[32:33]
	v_pk_mul_f32 v[58:59], v[2:3], v[30:31]
	v_pk_mul_f32 v[52:53], v[4:5], v[44:45]
	v_pk_mul_f32 v[50:51], v[2:3], v[42:43]
	v_pk_mul_f32 v[24:25], v[4:5], v[40:41]
	v_pk_mul_f32 v[22:23], v[2:3], v[38:39]
	v_pk_fma_f32 v[136:137], v[4:5], v[40:41], v[12:13]
	v_pk_fma_f32 v[138:139], v[2:3], v[38:39], v[10:11]
	s_waitcnt vmcnt(7)
	v_mov_b64_e32 v[48:49], v[20:21]
	s_waitcnt vmcnt(6)
	v_mov_b64_e32 v[44:45], v[8:9]
	s_waitcnt vmcnt(5)
	v_mov_b64_e32 v[38:39], v[62:63]
	s_waitcnt vmcnt(4)
	v_mov_b64_e32 v[34:35], v[54:55]
	s_waitcnt vmcnt(3)
	v_mov_b64_e32 v[30:31], v[78:79]
	s_waitcnt vmcnt(2)
	v_mov_b64_e32 v[26:27], v[70:71]
	s_waitcnt vmcnt(1)
	v_mov_b64_e32 v[14:15], v[94:95]
	s_waitcnt vmcnt(0)
	v_mov_b64_e32 v[10:11], v[86:87]
	v_mov_b64_e32 v[42:43], v[6:7]
	v_mov_b64_e32 v[46:47], v[18:19]
	v_mov_b64_e32 v[36:37], v[56:57]
	v_mov_b64_e32 v[40:41], v[64:65]
	v_mov_b64_e32 v[28:29], v[72:73]
	v_mov_b64_e32 v[32:33], v[80:81]
	v_mov_b64_e32 v[12:13], v[88:89]
	v_mov_b64_e32 v[16:17], v[96:97]
	s_cmp_eq_u32 s1, 56
	v_add_u32_e32 v134, s1, v186
	s_cbranch_scc1 .LBB0_290
	s_branch .LBB0_289

.LBB0_289:
	v_add_u32_e32 v10, 8, v134
	v_ashrrev_i32_e32 v11, 31, v10
	v_lshlrev_b64 v[10:11], 12, v[10:11]
	v_lshl_add_u64 v[26:27], v[166:167], 0, v[10:11]
	v_add_u32_e32 v10, 9, v134
	v_ashrrev_i32_e32 v11, 31, v10
	v_lshlrev_b64 v[10:11], 12, v[10:11]
	v_lshl_add_u64 v[28:29], v[166:167], 0, v[10:11]
	global_load_dwordx4 v[14:17], v[26:27], off nt
	global_load_dwordx4 v[10:13], v[28:29], off nt
	v_add_u32_e32 v26, 10, v134
	v_ashrrev_i32_e32 v27, 31, v26
	v_lshlrev_b64 v[26:27], 12, v[26:27]
	v_lshl_add_u64 v[34:35], v[166:167], 0, v[26:27]
	v_add_u32_e32 v26, 11, v134
	v_ashrrev_i32_e32 v27, 31, v26
	v_lshlrev_b64 v[26:27], 12, v[26:27]
	v_lshl_add_u64 v[36:37], v[166:167], 0, v[26:27]
	global_load_dwordx4 v[30:33], v[34:35], off nt
	global_load_dwordx4 v[26:29], v[36:37], off nt
	v_add_u32_e32 v34, 12, v134
	v_ashrrev_i32_e32 v35, 31, v34
	v_lshlrev_b64 v[34:35], 12, v[34:35]
	v_lshl_add_u64 v[42:43], v[166:167], 0, v[34:35]
	v_add_u32_e32 v34, 13, v134
	v_ashrrev_i32_e32 v35, 31, v34
	v_lshlrev_b64 v[34:35], 12, v[34:35]
	v_lshl_add_u64 v[44:45], v[166:167], 0, v[34:35]
	global_load_dwordx4 v[38:41], v[42:43], off nt
	global_load_dwordx4 v[34:37], v[44:45], off nt
	v_add_u32_e32 v42, 14, v134
	v_add_u32_e32 v44, 15, v134
	v_ashrrev_i32_e32 v43, 31, v42
	v_ashrrev_i32_e32 v45, 31, v44
	v_lshlrev_b64 v[42:43], 12, v[42:43]
	v_lshlrev_b64 v[44:45], 12, v[44:45]
	v_lshl_add_u64 v[42:43], v[166:167], 0, v[42:43]
	v_lshl_add_u64 v[44:45], v[166:167], 0, v[44:45]
	global_load_dwordx4 v[46:49], v[42:43], off nt
	s_nop 0
	global_load_dwordx4 v[42:45], v[44:45], off nt

.LBB0_296:
	v_mov_b32_e32 v6, 0
	s_waitcnt vmcnt(14)
	v_mov_b32_e32 v10, 0
	v_mov_b32_e32 v11, 0
	v_mov_b32_e32 v12, 0
	v_mov_b32_e32 v13, 0
	s_and_saveexec_b64 s[16:17], s[8:9]
	s_cbranch_execz .LBB0_298
	v_ashrrev_i32_e32 v171, 31, v170
	v_lshlrev_b64 v[8:9], 12, v[170:171]
	v_lshl_add_u64 v[8:9], v[166:167], 0, v[8:9]
	v_add_co_u32_e32 v8, vcc, 0xffff0000, v8
	s_nop 1
	v_addc_co_u32_e32 v9, vcc, -1, v9, vcc
	global_load_dwordx4 v[10:13], v[8:9], off nt
.LBB0_298:
	s_or_b64 exec, exec, s[16:17]
	v_mov_b32_e32 v7, 0
	v_mov_b32_e32 v8, 0
	v_mov_b32_e32 v9, 0
	s_and_saveexec_b64 s[16:17], s[8:9]
	s_cbranch_execz .LBB0_300
	v_ashrrev_i32_e32 v171, 31, v170
	v_lshlrev_b64 v[6:7], 12, v[170:171]
	v_lshl_add_u64 v[6:7], v[166:167], 0, v[6:7]
	v_add_co_u32_e32 v6, vcc, 0xffff1000, v6
	s_nop 1
	v_addc_co_u32_e32 v7, vcc, -1, v7, vcc
	global_load_dwordx4 v[6:9], v[6:7], off nt
.LBB0_300:
	s_or_b64 exec, exec, s[16:17]
	v_mov_b32_e32 v14, 0
	v_mov_b32_e32 v18, 0
	v_mov_b32_e32 v19, 0
	v_mov_b32_e32 v20, 0
	v_mov_b32_e32 v21, 0
	s_and_saveexec_b64 s[16:17], s[8:9]
	s_cbranch_execz .LBB0_302
	v_ashrrev_i32_e32 v171, 31, v170
	v_lshlrev_b64 v[16:17], 12, v[170:171]
	v_lshl_add_u64 v[16:17], v[166:167], 0, v[16:17]
	v_add_co_u32_e32 v16, vcc, 0xffff2000, v16
	s_nop 1
	v_addc_co_u32_e32 v17, vcc, -1, v17, vcc
	global_load_dwordx4 v[18:21], v[16:17], off nt
.LBB0_302:
	s_or_b64 exec, exec, s[16:17]
	v_mov_b32_e32 v15, 0
	v_mov_b32_e32 v16, 0
	v_mov_b32_e32 v17, 0
	s_and_saveexec_b64 s[16:17], s[8:9]
	s_cbranch_execz .LBB0_304
	v_ashrrev_i32_e32 v171, 31, v170
	v_lshlrev_b64 v[14:15], 12, v[170:171]
	v_lshl_add_u64 v[14:15], v[166:167], 0, v[14:15]
	v_add_co_u32_e32 v14, vcc, 0xffff3000, v14
	s_nop 1
	v_addc_co_u32_e32 v15, vcc, -1, v15, vcc
	global_load_dwordx4 v[14:17], v[14:15], off nt
.LBB0_304:
	s_or_b64 exec, exec, s[16:17]
	s_waitcnt vmcnt(12)
	v_mov_b32_e32 v26, 0
	s_waitcnt vmcnt(10)
	v_mov_b32_e32 v34, 0
	v_mov_b32_e32 v35, 0
	v_mov_b32_e32 v36, 0
	v_mov_b32_e32 v37, 0
	s_and_saveexec_b64 s[16:17], s[8:9]
	s_cbranch_execz .LBB0_306
	v_ashrrev_i32_e32 v171, 31, v170
	v_lshlrev_b64 v[22:23], 12, v[170:171]
	v_lshl_add_u64 v[22:23], v[166:167], 0, v[22:23]
	v_add_co_u32_e32 v22, vcc, 0xffff4000, v22
	s_nop 1
	v_addc_co_u32_e32 v23, vcc, -1, v23, vcc
	global_load_dwordx4 v[34:37], v[22:23], off nt
.LBB0_306:
	s_or_b64 exec, exec, s[16:17]
	v_mov_b32_e32 v27, 0
	v_mov_b32_e32 v28, 0
	v_mov_b32_e32 v29, 0
	s_and_saveexec_b64 s[16:17], s[8:9]
	s_cbranch_execz .LBB0_308
	v_ashrrev_i32_e32 v171, 31, v170
	v_lshlrev_b64 v[22:23], 12, v[170:171]
	v_lshl_add_u64 v[22:23], v[166:167], 0, v[22:23]
	v_add_co_u32_e32 v22, vcc, 0xffff5000, v22
	s_nop 1
	v_addc_co_u32_e32 v23, vcc, -1, v23, vcc
	global_load_dwordx4 v[26:29], v[22:23], off nt
.LBB0_308:
	s_or_b64 exec, exec, s[16:17]
	s_waitcnt vmcnt(8)
	v_mov_b32_e32 v42, 0
	v_mov_b32_e32 v50, 0
	v_mov_b32_e32 v51, 0
	v_mov_b32_e32 v52, 0
	v_mov_b32_e32 v53, 0
	s_and_saveexec_b64 s[16:17], s[8:9]
	s_cbranch_execz .LBB0_310
	v_ashrrev_i32_e32 v171, 31, v170
	v_lshlrev_b64 v[22:23], 12, v[170:171]
	v_lshl_add_u64 v[22:23], v[166:167], 0, v[22:23]
	v_add_co_u32_e32 v22, vcc, 0xffff6000, v22
	s_nop 1
	v_addc_co_u32_e32 v23, vcc, -1, v23, vcc
	global_load_dwordx4 v[50:53], v[22:23], off nt
.LBB0_310:
	s_or_b64 exec, exec, s[16:17]
	v_mov_b32_e32 v43, 0
	v_mov_b32_e32 v44, 0
	v_mov_b32_e32 v45, 0
	s_and_saveexec_b64 s[16:17], s[8:9]
	s_cbranch_execz .LBB0_312
	v_ashrrev_i32_e32 v171, 31, v170
	v_lshlrev_b64 v[22:23], 12, v[170:171]
	v_lshl_add_u64 v[22:23], v[166:167], 0, v[22:23]
	v_add_co_u32_e32 v22, vcc, 0xffff7000, v22
	s_nop 1
	v_addc_co_u32_e32 v23, vcc, -1, v23, vcc
	global_load_dwordx4 v[42:45], v[22:23], off nt

.LBB0_314:
	s_or_b64 exec, exec, s[16:17]
	s_waitcnt lgkmcnt(0)
	s_barrier
	ds_read_b128 v[98:101], v40
	ds_read_b128 v[94:97], v40 offset:16
	ds_read_b128 v[90:93], v40 offset:32
	ds_read_b128 v[78:81], v40 offset:48
	ds_read_b128 v[58:61], v40 offset:64
	ds_read_b128 v[54:57], v40 offset:80
	ds_read_b128 v[30:33], v40 offset:96
	ds_read_b128 v[22:25], v40 offset:112
	v_mov_b32_e32 v38, 0
	v_mov_b32_e32 v46, 0
	v_mov_b32_e32 v47, 0
	v_mov_b32_e32 v48, 0
	v_mov_b32_e32 v49, 0
	s_and_saveexec_b64 s[16:17], s[8:9]
	s_cbranch_execz .LBB0_316
	v_ashrrev_i32_e32 v171, 31, v170
	v_lshlrev_b64 v[40:41], 12, v[170:171]
	v_lshl_add_u64 v[40:41], v[166:167], 0, v[40:41]
	v_add_co_u32_e32 v40, vcc, 0xffff8000, v40
	s_nop 1
	v_addc_co_u32_e32 v41, vcc, -1, v41, vcc
	global_load_dwordx4 v[46:49], v[40:41], off nt
.LBB0_316:
	s_or_b64 exec, exec, s[16:17]
	v_mov_b32_e32 v39, 0
	v_mov_b32_e32 v40, 0
	v_mov_b32_e32 v41, 0
	s_and_saveexec_b64 s[16:17], s[8:9]
	s_cbranch_execz .LBB0_318
	v_ashrrev_i32_e32 v171, 31, v170
	v_lshlrev_b64 v[38:39], 12, v[170:171]
	v_lshl_add_u64 v[38:39], v[166:167], 0, v[38:39]
	v_add_co_u32_e32 v38, vcc, 0xffff9000, v38
	s_nop 1
	v_addc_co_u32_e32 v39, vcc, -1, v39, vcc
	global_load_dwordx4 v[38:41], v[38:39], off nt
.LBB0_318:
	s_or_b64 exec, exec, s[16:17]
	v_mov_b32_e32 v62, 0
	v_mov_b32_e32 v66, 0
	v_mov_b32_e32 v67, 0
	v_mov_b32_e32 v68, 0
	v_mov_b32_e32 v69, 0
	s_and_saveexec_b64 s[16:17], s[8:9]
	s_cbranch_execz .LBB0_320
	v_ashrrev_i32_e32 v171, 31, v170
	v_lshlrev_b64 v[64:65], 12, v[170:171]
	v_lshl_add_u64 v[64:65], v[166:167], 0, v[64:65]
	v_add_co_u32_e32 v64, vcc, 0xffffa000, v64
	s_nop 1
	v_addc_co_u32_e32 v65, vcc, -1, v65, vcc
	global_load_dwordx4 v[66:69], v[64:65], off nt
.LBB0_320:
	s_or_b64 exec, exec, s[16:17]
	v_mov_b32_e32 v63, 0
	v_mov_b32_e32 v64, 0
	v_mov_b32_e32 v65, 0
	s_and_saveexec_b64 s[16:17], s[8:9]
	s_cbranch_execz .LBB0_322
	v_ashrrev_i32_e32 v171, 31, v170
	v_lshlrev_b64 v[62:63], 12, v[170:171]
	v_lshl_add_u64 v[62:63], v[166:167], 0, v[62:63]
	v_add_co_u32_e32 v62, vcc, 0xffffb000, v62
	s_nop 1
	v_addc_co_u32_e32 v63, vcc, -1, v63, vcc
	global_load_dwordx4 v[62:65], v[62:63], off nt
.LBB0_322:
	s_or_b64 exec, exec, s[16:17]
	v_mov_b32_e32 v70, 0
	v_mov_b32_e32 v74, 0
	v_mov_b32_e32 v75, 0
	v_mov_b32_e32 v76, 0
	v_mov_b32_e32 v77, 0
	s_and_saveexec_b64 s[16:17], s[8:9]
	s_cbranch_execz .LBB0_324
	v_ashrrev_i32_e32 v171, 31, v170
	v_lshlrev_b64 v[72:73], 12, v[170:171]
	v_lshl_add_u64 v[72:73], v[166:167], 0, v[72:73]
	v_add_co_u32_e32 v72, vcc, 0xffffc000, v72
	s_nop 1
	v_addc_co_u32_e32 v73, vcc, -1, v73, vcc
	global_load_dwordx4 v[74:77], v[72:73], off nt
.LBB0_324:
	s_or_b64 exec, exec, s[16:17]
	v_mov_b32_e32 v71, 0
	v_mov_b32_e32 v72, 0
	v_mov_b32_e32 v73, 0
	s_and_saveexec_b64 s[16:17], s[8:9]
	s_cbranch_execz .LBB0_326
	v_ashrrev_i32_e32 v171, 31, v170
	v_lshlrev_b64 v[70:71], 12, v[170:171]
	v_lshl_add_u64 v[70:71], v[166:167], 0, v[70:71]
	v_add_co_u32_e32 v70, vcc, 0xffffd000, v70
	s_nop 1
	v_addc_co_u32_e32 v71, vcc, -1, v71, vcc
	global_load_dwordx4 v[70:73], v[70:71], off nt
.LBB0_326:
	s_or_b64 exec, exec, s[16:17]
	v_mov_b32_e32 v82, 0
	v_mov_b32_e32 v86, 0
	v_mov_b32_e32 v87, 0
	v_mov_b32_e32 v88, 0
	v_mov_b32_e32 v89, 0
	s_and_saveexec_b64 s[16:17], s[8:9]
	s_cbranch_execz .LBB0_328
	v_ashrrev_i32_e32 v171, 31, v170
	v_lshlrev_b64 v[84:85], 12, v[170:171]
	v_lshl_add_u64 v[84:85], v[166:167], 0, v[84:85]
	v_add_co_u32_e32 v84, vcc, 0xffffe000, v84
	s_nop 1
	v_addc_co_u32_e32 v85, vcc, -1, v85, vcc
	global_load_dwordx4 v[86:89], v[84:85], off nt
.LBB0_328:
	s_or_b64 exec, exec, s[16:17]
	v_mov_b32_e32 v83, 0
	v_mov_b32_e32 v84, 0
	v_mov_b32_e32 v85, 0
	s_and_saveexec_b64 s[16:17], s[8:9]
	s_cbranch_execz .LBB0_330
	v_ashrrev_i32_e32 v171, 31, v170
	v_lshlrev_b64 v[82:83], 12, v[170:171]
	v_lshl_add_u64 v[82:83], v[166:167], 0, v[82:83]
	global_load_dwordx4 v[82:85], v[82:83], off offset:-4096 nt

.LBB0_332:
	s_or_b64 exec, exec, s[16:17]
	v_mov_b32_e32 v102, v99
	s_waitcnt lgkmcnt(7)
	v_mov_b32_e32 v103, v100
	v_mov_b32_e32 v99, v101
	v_mov_b32_e32 v100, v95
	v_mov_b32_e32 v101, v96
	v_mov_b32_e32 v95, v97
	v_pk_add_f32 v[94:95], v[100:101], v[94:95]
	s_waitcnt lgkmcnt(0)
	v_add_f32_e32 v94, v94, v95
	v_fmamk_f32 v94, v94, 0x3a800000, v187
	v_rsq_f32_e32 v100, v94
	v_mov_b32_e32 v94, v91
	v_mov_b32_e32 v95, v92
	v_mov_b32_e32 v91, v93
	v_mov_b32_e32 v92, v79
	v_mov_b32_e32 v93, v80
	v_mov_b32_e32 v79, v81
	v_pk_add_f32 v[78:79], v[92:93], v[78:79]
	s_barrier
	v_add_f32_e32 v78, v78, v79
	v_fmamk_f32 v78, v78, 0x3a800000, v187
	v_rsq_f32_e32 v92, v78
	v_mov_b32_e32 v78, v59
	v_mov_b32_e32 v79, v60
	v_mov_b32_e32 v59, v61
	v_mov_b32_e32 v60, v55
	v_mov_b32_e32 v61, v56
	v_mov_b32_e32 v55, v57
	v_pk_add_f32 v[54:55], v[60:61], v[54:55]
	v_pk_add_f32 v[58:59], v[78:79], v[58:59]
	v_add_f32_e32 v54, v54, v55
	v_fmamk_f32 v54, v54, 0x3a800000, v187
	v_rsq_f32_e32 v60, v54
	v_mov_b32_e32 v54, v31
	v_mov_b32_e32 v55, v32
	v_mov_b32_e32 v31, v33
	v_pk_add_f32 v[30:31], v[54:55], v[30:31]
	v_add_f32_e32 v58, v58, v59
	v_add_f32_e32 v30, v30, v31
	v_fmamk_f32 v30, v30, 0x3a800000, v187
	v_rsq_f32_e32 v112, v30
	v_mov_b32_e32 v30, v23
	v_mov_b32_e32 v31, v24
	v_mov_b32_e32 v23, v25
	v_pk_add_f32 v[22:23], v[30:31], v[22:23]
	v_fmamk_f32 v58, v58, 0x3a800000, v187
	v_add_f32_e32 v22, v22, v23
	v_fmamk_f32 v22, v22, 0x3a800000, v187
	v_rsq_f32_e32 v58, v58
	v_rsq_f32_e32 v114, v22
	v_pk_mul_f32 v[138:139], v[26:27], v[60:61] op_sel_hi:[1,0]
	v_pk_mul_f32 v[140:141], v[28:29], v[60:61] op_sel_hi:[1,0]
	ds_read_b128 v[26:29], v110
	v_pk_mul_f32 v[134:135], v[34:35], v[58:59] op_sel_hi:[1,0]
	v_pk_mul_f32 v[136:137], v[36:37], v[58:59] op_sel_hi:[1,0]
	v_pk_mul_f32 v[142:143], v[50:51], v[112:113] op_sel_hi:[1,0]
	v_pk_mul_f32 v[144:145], v[52:53], v[112:113] op_sel_hi:[1,0]
	v_pk_mul_f32 v[146:147], v[42:43], v[114:115] op_sel_hi:[1,0]
	v_pk_mul_f32 v[148:149], v[44:45], v[114:115] op_sel_hi:[1,0]
	ds_read_b128 v[34:37], v110 offset:16
	ds_read_b128 v[42:45], v110 offset:32
	ds_read_b128 v[50:53], v110 offset:48
	s_waitcnt lgkmcnt(3)
	v_mov_b32_e32 v58, v27
	v_mov_b32_e32 v59, v28
	v_mov_b32_e32 v27, v29
	s_waitcnt lgkmcnt(2)
	v_mov_b32_e32 v28, v35
	v_mov_b32_e32 v29, v36
	v_mov_b32_e32 v35, v37
	v_pk_add_f32 v[26:27], v[58:59], v[26:27]
	v_pk_add_f32 v[28:29], v[28:29], v[34:35]
	v_add_f32_e32 v26, v26, v27
	v_add_f32_e32 v27, v28, v29
	s_waitcnt lgkmcnt(1)
	v_mov_b32_e32 v28, v43
	v_mov_b32_e32 v29, v44
	v_mov_b32_e32 v43, v45
	v_fmamk_f32 v27, v27, 0x3a800000, v187
	v_pk_add_f32 v[28:29], v[28:29], v[42:43]
	v_rsq_f32_e32 v34, v27
	v_add_f32_e32 v27, v28, v29
	s_waitcnt lgkmcnt(0)
	v_mov_b32_e32 v28, v51
	v_mov_b32_e32 v29, v52
	v_mov_b32_e32 v51, v53
	v_pk_add_f32 v[28:29], v[28:29], v[50:51]
	ds_read_b128 v[50:53], v110 offset:64
	ds_read_b128 v[58:61], v110 offset:80
	v_fmamk_f32 v27, v27, 0x3a800000, v187
	v_rsq_f32_e32 v36, v27
	v_add_f32_e32 v27, v28, v29
	s_waitcnt lgkmcnt(1)
	v_mov_b32_e32 v28, v51
	v_mov_b32_e32 v29, v52
	v_mov_b32_e32 v51, v53
	v_fmamk_f32 v27, v27, 0x3a800000, v187
	v_pk_add_f32 v[28:29], v[28:29], v[50:51]
	v_rsq_f32_e32 v42, v27
	v_add_f32_e32 v27, v28, v29
	s_waitcnt lgkmcnt(0)
	v_mov_b32_e32 v28, v59
	v_mov_b32_e32 v29, v60
	v_mov_b32_e32 v59, v61
	v_pk_add_f32 v[28:29], v[28:29], v[58:59]
	v_or_b32_e32 v58, 2, v170
	v_ashrrev_i32_e32 v59, 31, v58
	v_lshlrev_b64 v[58:59], 12, v[58:59]
	v_lshl_add_u64 v[118:119], v[166:167], 0, v[58:59]
	v_or_b32_e32 v58, 3, v170
	v_ashrrev_i32_e32 v59, 31, v58
	v_lshlrev_b64 v[58:59], 12, v[58:59]
	v_lshl_add_u64 v[120:121], v[166:167], 0, v[58:59]
	v_or_b32_e32 v58, 4, v170
	v_ashrrev_i32_e32 v59, 31, v58
	ds_read_b128 v[50:53], v110 offset:96
	ds_read_b128 v[150:153], v110 offset:112
	v_lshlrev_b64 v[58:59], 12, v[58:59]
	v_pk_add_f32 v[90:91], v[94:95], v[90:91]
	v_lshl_add_u64 v[110:111], v[166:167], 0, v[58:59]
	v_or_b32_e32 v58, 5, v170
	v_add_f32_e32 v90, v90, v91
	v_ashrrev_i32_e32 v59, 31, v58
	v_fmamk_f32 v90, v90, 0x3a800000, v187
	v_lshlrev_b64 v[58:59], 12, v[58:59]
	v_rsq_f32_e32 v90, v90
	v_fmamk_f32 v27, v27, 0x3a800000, v187
	v_lshl_add_u64 v[112:113], v[166:167], 0, v[58:59]
	v_or_b32_e32 v58, 6, v170
	v_or_b32_e32 v60, 7, v170
	v_rsq_f32_e32 v44, v27
	v_add_f32_e32 v27, v28, v29
	s_waitcnt lgkmcnt(1)
	v_mov_b32_e32 v28, v51
	v_mov_b32_e32 v29, v52
	v_mov_b32_e32 v51, v53
	v_or_b32_e32 v52, 1, v170
	v_ashrrev_i32_e32 v59, 31, v58
	v_ashrrev_i32_e32 v61, 31, v60
	v_fmamk_f32 v27, v27, 0x3a800000, v187
	v_pk_add_f32 v[28:29], v[28:29], v[50:51]
	v_ashrrev_i32_e32 v171, 31, v170
	v_ashrrev_i32_e32 v53, 31, v52
	v_lshlrev_b64 v[58:59], 12, v[58:59]
	v_lshlrev_b64 v[60:61], 12, v[60:61]
	v_rsq_f32_e32 v154, v27
	v_add_f32_e32 v27, v28, v29
	v_lshlrev_b64 v[28:29], 12, v[170:171]
	v_lshlrev_b64 v[52:53], 12, v[52:53]
	v_lshl_add_u64 v[58:59], v[166:167], 0, v[58:59]
	v_lshl_add_u64 v[60:61], v[166:167], 0, v[60:61]
	v_pk_add_f32 v[98:99], v[102:103], v[98:99]
	v_pk_mul_f32 v[102:103], v[18:19], v[90:91] op_sel_hi:[1,0]
	v_pk_mul_f32 v[104:105], v[20:21], v[90:91] op_sel_hi:[1,0]
	v_pk_mul_f32 v[106:107], v[14:15], v[92:93] op_sel_hi:[1,0]
	v_pk_mul_f32 v[108:109], v[16:17], v[92:93] op_sel_hi:[1,0]
	v_lshl_add_u64 v[28:29], v[166:167], 0, v[28:29]
	v_lshl_add_u64 v[52:53], v[166:167], 0, v[52:53]
	global_load_dwordx4 v[90:93], v[58:59], off nt
	s_nop 0
	global_load_dwordx4 v[58:61], v[60:61], off nt
	s_nop 0
	global_load_dwordx4 v[114:117], v[110:111], off nt
	s_nop 0
	global_load_dwordx4 v[110:113], v[112:113], off nt
	s_nop 0
	global_load_dwordx4 v[122:125], v[118:119], off nt
	s_nop 0
	global_load_dwordx4 v[118:121], v[120:121], off nt
	s_nop 0
	global_load_dwordx4 v[130:133], v[28:29], off nt
	global_load_dwordx4 v[126:129], v[52:53], off nt
	v_add_f32_e32 v98, v98, v99
	v_fmamk_f32 v98, v98, 0x3a800000, v187
	v_rsq_f32_e32 v98, v98
	v_fmamk_f32 v27, v27, 0x3a800000, v187
	v_rsq_f32_e32 v50, v27
	v_pk_mul_f32 v[164:165], v[62:63], v[42:43] op_sel_hi:[1,0]
	v_pk_mul_f32 v[96:97], v[12:13], v[98:99] op_sel_hi:[1,0]
	v_pk_mul_f32 v[94:95], v[10:11], v[98:99] op_sel_hi:[1,0]
	v_pk_mul_f32 v[98:99], v[6:7], v[100:101] op_sel_hi:[1,0]
	v_pk_mul_f32 v[100:101], v[8:9], v[100:101] op_sel_hi:[1,0]
	v_pk_mul_f32 v[86:87], v[86:87], v[50:51] op_sel_hi:[1,0]
	v_pk_mul_f32 v[88:89], v[88:89], v[50:51] op_sel_hi:[1,0]
	v_pk_fma_f32 v[50:51], v[4:5], v[96:97], 0 op_sel_hi:[1,1,0]
	v_pk_mul_f32 v[172:173], v[64:65], v[42:43] op_sel_hi:[1,0]
	v_pk_fma_f32 v[62:63], v[4:5], v[100:101], v[50:51]
	v_pk_fma_f32 v[50:51], v[2:3], v[94:95], 0 op_sel_hi:[1,1,0]
	v_fmamk_f32 v26, v26, 0x3a800000, v187
	v_pk_fma_f32 v[64:65], v[2:3], v[98:99], v[50:51]
	v_pk_mul_f32 v[160:161], v[66:67], v[36:37] op_sel_hi:[1,0]
	v_pk_mul_f32 v[162:163], v[68:69], v[36:37] op_sel_hi:[1,0]
	v_pk_fma_f32 v[66:67], v[2:3], v[102:103], v[64:65]
	v_pk_fma_f32 v[68:69], v[4:5], v[104:105], v[62:63]
	v_pk_mul_f32 v[80:81], v[4:5], v[96:97]
	v_pk_mul_f32 v[78:79], v[2:3], v[94:95]
	v_rsq_f32_e32 v26, v26
	s_waitcnt lgkmcnt(0)
	v_mov_b32_e32 v28, v151
	v_mov_b32_e32 v29, v152
	v_mov_b32_e32 v151, v153
	v_pk_fma_f32 v[94:95], v[4:5], v[108:109], v[68:69]
	v_pk_fma_f32 v[96:97], v[2:3], v[106:107], v[66:67]
	v_pk_add_f32 v[28:29], v[28:29], v[150:151]
	v_pk_fma_f32 v[96:97], v[2:3], v[134:135], v[96:97]
	v_pk_fma_f32 v[94:95], v[4:5], v[136:137], v[94:95]
	v_add_f32_e32 v27, v28, v29
	v_pk_fma_f32 v[94:95], v[4:5], v[140:141], v[94:95]
	v_pk_fma_f32 v[96:97], v[2:3], v[138:139], v[96:97]
	v_fmamk_f32 v27, v27, 0x3a800000, v187
	v_pk_fma_f32 v[96:97], v[2:3], v[142:143], v[96:97]
	v_pk_fma_f32 v[94:95], v[4:5], v[144:145], v[94:95]
	v_pk_mul_f32 v[150:151], v[46:47], v[26:27] op_sel_hi:[1,0]
	v_pk_mul_f32 v[152:153], v[48:49], v[26:27] op_sel_hi:[1,0]
	v_pk_fma_f32 v[94:95], v[4:5], v[148:149], v[94:95]
	v_pk_fma_f32 v[96:97], v[2:3], v[146:147], v[96:97]
	v_pk_mul_f32 v[156:157], v[38:39], v[34:35] op_sel_hi:[1,0]
	v_pk_mul_f32 v[158:159], v[40:41], v[34:35] op_sel_hi:[1,0]
	v_pk_fma_f32 v[96:97], v[2:3], v[150:151], v[96:97]
	v_pk_fma_f32 v[94:95], v[4:5], v[152:153], v[94:95]
	v_rsq_f32_e32 v52, v27
	v_pk_fma_f32 v[94:95], v[4:5], v[158:159], v[94:95]
	v_pk_fma_f32 v[96:97], v[2:3], v[156:157], v[96:97]
	v_pk_fma_f32 v[94:95], v[4:5], v[162:163], v[94:95]
	v_pk_fma_f32 v[96:97], v[2:3], v[160:161], v[96:97]
	v_pk_mul_f32 v[74:75], v[74:75], v[44:45] op_sel_hi:[1,0]
	v_pk_mul_f32 v[76:77], v[76:77], v[44:45] op_sel_hi:[1,0]
	v_pk_fma_f32 v[94:95], v[4:5], v[172:173], v[94:95]
	v_pk_fma_f32 v[96:97], v[2:3], v[164:165], v[96:97]
	v_pk_mul_f32 v[70:71], v[70:71], v[154:155] op_sel_hi:[1,0]
	v_pk_mul_f32 v[72:73], v[72:73], v[154:155] op_sel_hi:[1,0]
	v_pk_mul_f32 v[48:49], v[4:5], v[76:77]
	v_pk_mul_f32 v[46:47], v[2:3], v[74:75]
	v_pk_fma_f32 v[74:75], v[2:3], v[74:75], v[96:97]
	v_pk_fma_f32 v[76:77], v[4:5], v[76:77], v[94:95]
	v_pk_mul_f32 v[82:83], v[82:83], v[52:53] op_sel_hi:[1,0]
	v_pk_mul_f32 v[84:85], v[84:85], v[52:53] op_sel_hi:[1,0]
	v_pk_mul_f32 v[52:53], v[4:5], v[72:73]
	v_pk_mul_f32 v[50:51], v[2:3], v[70:71]
	v_pk_fma_f32 v[72:73], v[4:5], v[72:73], v[76:77]
	v_pk_fma_f32 v[70:71], v[2:3], v[70:71], v[74:75]
	v_pk_fma_f32 v[72:73], v[4:5], v[88:89], v[72:73]
	v_pk_fma_f32 v[70:71], v[2:3], v[86:87], v[70:71]
	v_pk_mul_f32 v[56:57], v[4:5], v[100:101]
	v_pk_mul_f32 v[54:55], v[2:3], v[98:99]
	v_pk_mul_f32 v[32:33], v[4:5], v[104:105]
	v_pk_mul_f32 v[30:31], v[2:3], v[102:103]
	v_pk_mul_f32 v[24:25], v[4:5], v[108:109]
	v_pk_mul_f32 v[22:23], v[2:3], v[106:107]
	v_pk_mul_f32 v[64:65], v[4:5], v[88:89]
	v_pk_mul_f32 v[62:63], v[2:3], v[86:87]
	v_pk_mul_f32 v[68:69], v[4:5], v[84:85]
	v_pk_mul_f32 v[66:67], v[2:3], v[82:83]
	v_pk_fma_f32 v[174:175], v[4:5], v[84:85], v[72:73]
	v_pk_fma_f32 v[176:177], v[2:3], v[82:83], v[70:71]
	s_waitcnt vmcnt(6)
	v_mov_b64_e32 v[104:105], v[60:61]
	v_mov_b64_e32 v[108:109], v[92:93]
	s_waitcnt vmcnt(4)
	v_mov_b64_e32 v[94:95], v[110:111]
	v_mov_b64_e32 v[98:99], v[114:115]
	s_waitcnt vmcnt(2)
	v_mov_b64_e32 v[82:83], v[118:119]
	v_mov_b64_e32 v[86:87], v[122:123]
	s_waitcnt vmcnt(0)
	v_mov_b64_e32 v[70:71], v[126:127]
	v_mov_b64_e32 v[74:75], v[130:131]
	v_pk_mul_f32 v[20:21], v[4:5], v[136:137]
	v_pk_mul_f32 v[18:19], v[2:3], v[134:135]
	v_pk_mul_f32 v[16:17], v[4:5], v[140:141]
	v_pk_mul_f32 v[14:15], v[2:3], v[138:139]
	v_pk_mul_f32 v[12:13], v[4:5], v[144:145]
	v_pk_mul_f32 v[10:11], v[2:3], v[142:143]
	v_pk_mul_f32 v[8:9], v[4:5], v[148:149]
	v_pk_mul_f32 v[6:7], v[2:3], v[146:147]
	v_pk_mul_f32 v[28:29], v[4:5], v[152:153]
	v_pk_mul_f32 v[26:27], v[2:3], v[150:151]
	v_pk_mul_f32 v[36:37], v[4:5], v[158:159]
	v_pk_mul_f32 v[34:35], v[2:3], v[156:157]
	v_pk_mul_f32 v[40:41], v[4:5], v[162:163]
	v_pk_mul_f32 v[38:39], v[2:3], v[160:161]
	v_pk_mul_f32 v[44:45], v[4:5], v[172:173]
	v_pk_mul_f32 v[42:43], v[2:3], v[164:165]
	s_mov_b32 s1, 0
	s_mov_b32 s0, s23
	v_mov_b64_e32 v[102:103], v[58:59]
	v_mov_b64_e32 v[106:107], v[90:91]
	v_mov_b64_e32 v[96:97], v[112:113]
	v_mov_b64_e32 v[100:101], v[116:117]
	v_mov_b64_e32 v[84:85], v[120:121]
	v_mov_b64_e32 v[88:89], v[124:125]
	v_mov_b64_e32 v[72:73], v[128:129]
	v_mov_b64_e32 v[76:77], v[132:133]
	s_cmp_eq_u32 s1, 56
	v_add_u32_e32 v172, s1, v186
	s_cbranch_scc1 .LBB0_335
	s_branch .LBB0_334

.LBB0_334:
	v_add_u32_e32 v70, 8, v172
	v_add_u32_e32 v72, 9, v172
	v_add_u32_e32 v82, 10, v172
	v_add_u32_e32 v84, 11, v172
	v_add_u32_e32 v94, 12, v172
	v_add_u32_e32 v96, 13, v172
	v_add_u32_e32 v102, 14, v172
	v_add_u32_e32 v104, 15, v172
	v_ashrrev_i32_e32 v71, 31, v70
	v_ashrrev_i32_e32 v73, 31, v72
	v_ashrrev_i32_e32 v83, 31, v82
	v_ashrrev_i32_e32 v85, 31, v84
	v_ashrrev_i32_e32 v95, 31, v94
	v_ashrrev_i32_e32 v97, 31, v96
	v_ashrrev_i32_e32 v103, 31, v102
	v_ashrrev_i32_e32 v105, 31, v104
	v_lshlrev_b64 v[70:71], 12, v[70:71]
	v_lshlrev_b64 v[72:73], 12, v[72:73]
	v_lshlrev_b64 v[82:83], 12, v[82:83]
	v_lshlrev_b64 v[84:85], 12, v[84:85]
	v_lshlrev_b64 v[94:95], 12, v[94:95]
	v_lshlrev_b64 v[96:97], 12, v[96:97]
	v_lshlrev_b64 v[102:103], 12, v[102:103]
	v_lshlrev_b64 v[104:105], 12, v[104:105]
	v_lshl_add_u64 v[70:71], v[166:167], 0, v[70:71]
	v_lshl_add_u64 v[72:73], v[166:167], 0, v[72:73]
	v_lshl_add_u64 v[82:83], v[166:167], 0, v[82:83]
	v_lshl_add_u64 v[84:85], v[166:167], 0, v[84:85]
	v_lshl_add_u64 v[94:95], v[166:167], 0, v[94:95]
	v_lshl_add_u64 v[96:97], v[166:167], 0, v[96:97]
	v_lshl_add_u64 v[102:103], v[166:167], 0, v[102:103]
	v_lshl_add_u64 v[104:105], v[166:167], 0, v[104:105]
	global_load_dwordx4 v[74:77], v[70:71], off nt
	s_nop 0
	global_load_dwordx4 v[70:73], v[72:73], off nt
	s_nop 0
	global_load_dwordx4 v[86:89], v[82:83], off nt
	s_nop 0
	global_load_dwordx4 v[82:85], v[84:85], off nt
	s_nop 0
	global_load_dwordx4 v[98:101], v[94:95], off nt
	s_nop 0
	global_load_dwordx4 v[94:97], v[96:97], off nt
	s_nop 0
	global_load_dwordx4 v[106:109], v[102:103], off nt
	s_nop 0
	global_load_dwordx4 v[102:105], v[104:105], off nt

.LBB0_341:
	s_and_b64 vcc, exec, s[16:17]
	s_cbranch_vccz .LBB0_384
	v_mov_b32_e32 v6, 0
	s_waitcnt vmcnt(14)
	v_mov_b32_e32 v10, 0
	v_mov_b32_e32 v11, 0
	v_mov_b32_e32 v12, 0
	v_mov_b32_e32 v13, 0
	s_and_saveexec_b64 s[16:17], s[8:9]
	s_cbranch_execz .LBB0_344
	v_ashrrev_i32_e32 v171, 31, v170
	v_lshlrev_b64 v[8:9], 12, v[170:171]
	v_lshl_add_u64 v[8:9], v[166:167], 0, v[8:9]
	v_add_co_u32_e32 v8, vcc, 0xffff0000, v8
	s_nop 1
	v_addc_co_u32_e32 v9, vcc, -1, v9, vcc
	global_load_dwordx4 v[10:13], v[8:9], off nt

.LBB0_346:
	s_or_b64 exec, exec, s[16:17]
	v_mov_b32_e32 v14, 0
	s_waitcnt vmcnt(12)
	v_mov_b32_e32 v22, 0
	v_mov_b32_e32 v23, 0
	v_mov_b32_e32 v24, 0
	v_mov_b32_e32 v25, 0
	s_and_saveexec_b64 s[16:17], s[8:9]
	s_cbranch_execz .LBB0_348
	v_ashrrev_i32_e32 v171, 31, v170
	v_lshlrev_b64 v[16:17], 12, v[170:171]
	v_lshl_add_u64 v[16:17], v[166:167], 0, v[16:17]
	v_add_co_u32_e32 v16, vcc, 0xffff2000, v16
	s_nop 1
	v_addc_co_u32_e32 v17, vcc, -1, v17, vcc
	global_load_dwordx4 v[22:25], v[16:17], off nt

.LBB0_350:
	s_or_b64 exec, exec, s[16:17]
	v_mov_b32_e32 v18, 0
	s_waitcnt vmcnt(10)
	v_mov_b32_e32 v30, 0
	v_mov_b32_e32 v31, 0
	v_mov_b32_e32 v32, 0
	v_mov_b32_e32 v33, 0
	s_and_saveexec_b64 s[16:17], s[8:9]
	s_cbranch_execz .LBB0_352
	v_ashrrev_i32_e32 v171, 31, v170
	v_lshlrev_b64 v[20:21], 12, v[170:171]
	v_lshl_add_u64 v[20:21], v[166:167], 0, v[20:21]
	v_add_co_u32_e32 v20, vcc, 0xffff4000, v20
	s_nop 1
	v_addc_co_u32_e32 v21, vcc, -1, v21, vcc
	global_load_dwordx4 v[30:33], v[20:21], off nt
.LBB0_352:
	s_or_b64 exec, exec, s[16:17]
	v_mov_b32_e32 v19, 0
	v_mov_b32_e32 v20, 0
	v_mov_b32_e32 v21, 0
	s_and_saveexec_b64 s[16:17], s[8:9]
	s_cbranch_execz .LBB0_354
	v_ashrrev_i32_e32 v171, 31, v170
	v_lshlrev_b64 v[18:19], 12, v[170:171]
	v_lshl_add_u64 v[18:19], v[166:167], 0, v[18:19]
	v_add_co_u32_e32 v18, vcc, 0xffff5000, v18
	s_nop 1
	v_addc_co_u32_e32 v19, vcc, -1, v19, vcc
	global_load_dwordx4 v[18:21], v[18:19], off nt
.LBB0_354:
	s_or_b64 exec, exec, s[16:17]
	s_waitcnt vmcnt(12)
	v_mov_b32_e32 v26, 0
	s_waitcnt vmcnt(10)
	v_mov_b32_e32 v34, 0
	v_mov_b32_e32 v35, 0
	v_mov_b32_e32 v36, 0
	v_mov_b32_e32 v37, 0
	s_and_saveexec_b64 s[16:17], s[8:9]
	s_cbranch_execz .LBB0_356
	v_ashrrev_i32_e32 v171, 31, v170
	v_lshlrev_b64 v[28:29], 12, v[170:171]
	v_lshl_add_u64 v[28:29], v[166:167], 0, v[28:29]
	v_add_co_u32_e32 v28, vcc, 0xffff6000, v28
	s_nop 1
	v_addc_co_u32_e32 v29, vcc, -1, v29, vcc
	global_load_dwordx4 v[34:37], v[28:29], off nt
.LBB0_356:
	s_or_b64 exec, exec, s[16:17]
	v_mov_b32_e32 v27, 0
	v_mov_b32_e32 v28, 0
	v_mov_b32_e32 v29, 0
	s_and_saveexec_b64 s[16:17], s[8:9]
	s_cbranch_execz .LBB0_358
	v_ashrrev_i32_e32 v171, 31, v170
	v_lshlrev_b64 v[26:27], 12, v[170:171]
	v_lshl_add_u64 v[26:27], v[166:167], 0, v[26:27]
	v_add_co_u32_e32 v26, vcc, 0xffff7000, v26
	s_nop 1
	v_addc_co_u32_e32 v27, vcc, -1, v27, vcc
	global_load_dwordx4 v[26:29], v[26:27], off nt

.LBB0_360:
	s_or_b64 exec, exec, s[16:17]
	v_mov_b32_e32 v6, 0
	v_mov_b32_e32 v10, 0
	s_waitcnt lgkmcnt(5)
	v_mov_b32_e32 v11, 0
	v_mov_b32_e32 v12, 0
	s_waitcnt lgkmcnt(4)
	v_mov_b32_e32 v13, 0
	s_waitcnt lgkmcnt(0)
	s_barrier
	s_and_saveexec_b64 s[16:17], s[8:9]
	s_cbranch_execz .LBB0_362
	v_ashrrev_i32_e32 v171, 31, v170
	v_lshlrev_b64 v[8:9], 12, v[170:171]
	v_lshl_add_u64 v[8:9], v[166:167], 0, v[8:9]
	v_add_co_u32_e32 v8, vcc, 0xffff8000, v8
	s_nop 1
	v_addc_co_u32_e32 v9, vcc, -1, v9, vcc
	global_load_dwordx4 v[10:13], v[8:9], off nt
.LBB0_362:
	s_or_b64 exec, exec, s[16:17]
	v_mov_b32_e32 v7, 0
	v_mov_b32_e32 v8, 0
	v_mov_b32_e32 v9, 0
	s_and_saveexec_b64 s[16:17], s[8:9]
	s_cbranch_execz .LBB0_364
	v_ashrrev_i32_e32 v171, 31, v170
	v_lshlrev_b64 v[6:7], 12, v[170:171]
	v_lshl_add_u64 v[6:7], v[166:167], 0, v[6:7]
	v_add_co_u32_e32 v6, vcc, 0xffff9000, v6
	s_nop 1
	v_addc_co_u32_e32 v7, vcc, -1, v7, vcc
	global_load_dwordx4 v[6:9], v[6:7], off nt
.LBB0_364:
	s_or_b64 exec, exec, s[16:17]
	v_mov_b32_e32 v30, 0
	v_mov_b32_e32 v34, 0
	v_mov_b32_e32 v35, 0
	v_mov_b32_e32 v36, 0
	v_mov_b32_e32 v37, 0
	s_and_saveexec_b64 s[16:17], s[8:9]
	s_cbranch_execz .LBB0_366
	v_ashrrev_i32_e32 v171, 31, v170
	v_lshlrev_b64 v[14:15], 12, v[170:171]
	v_lshl_add_u64 v[14:15], v[166:167], 0, v[14:15]
	v_add_co_u32_e32 v14, vcc, 0xffffa000, v14
	s_nop 1
	v_addc_co_u32_e32 v15, vcc, -1, v15, vcc
	global_load_dwordx4 v[34:37], v[14:15], off nt
.LBB0_366:
	s_or_b64 exec, exec, s[16:17]
	v_mov_b32_e32 v31, 0
	v_mov_b32_e32 v32, 0
	v_mov_b32_e32 v33, 0
	s_and_saveexec_b64 s[16:17], s[8:9]
	s_cbranch_execz .LBB0_368
	v_ashrrev_i32_e32 v171, 31, v170
	v_lshlrev_b64 v[14:15], 12, v[170:171]
	v_lshl_add_u64 v[14:15], v[166:167], 0, v[14:15]
	v_add_co_u32_e32 v14, vcc, 0xffffb000, v14
	s_nop 1
	v_addc_co_u32_e32 v15, vcc, -1, v15, vcc
	global_load_dwordx4 v[30:33], v[14:15], off nt
.LBB0_368:
	s_or_b64 exec, exec, s[16:17]
	v_mov_b32_e32 v14, 0
	v_mov_b32_e32 v18, 0
	v_mov_b32_e32 v19, 0
	v_mov_b32_e32 v20, 0
	v_mov_b32_e32 v21, 0
	s_and_saveexec_b64 s[16:17], s[8:9]
	s_cbranch_execz .LBB0_370
	v_ashrrev_i32_e32 v171, 31, v170
	v_lshlrev_b64 v[16:17], 12, v[170:171]
	v_lshl_add_u64 v[16:17], v[166:167], 0, v[16:17]
	v_add_co_u32_e32 v16, vcc, 0xffffc000, v16
	s_nop 1
	v_addc_co_u32_e32 v17, vcc, -1, v17, vcc
	global_load_dwordx4 v[18:21], v[16:17], off nt
.LBB0_370:
	s_or_b64 exec, exec, s[16:17]
	v_mov_b32_e32 v15, 0
	v_mov_b32_e32 v16, 0
	v_mov_b32_e32 v17, 0
	s_and_saveexec_b64 s[16:17], s[8:9]
	s_cbranch_execz .LBB0_372
	v_ashrrev_i32_e32 v171, 31, v170
	v_lshlrev_b64 v[14:15], 12, v[170:171]
	v_lshl_add_u64 v[14:15], v[166:167], 0, v[14:15]
	v_add_co_u32_e32 v14, vcc, 0xffffd000, v14
	s_nop 1
	v_addc_co_u32_e32 v15, vcc, -1, v15, vcc
	global_load_dwordx4 v[14:17], v[14:15], off nt
.LBB0_372:
	s_or_b64 exec, exec, s[16:17]
	v_mov_b32_e32 v22, 0
	v_mov_b32_e32 v26, 0
	v_mov_b32_e32 v27, 0
	v_mov_b32_e32 v28, 0
	v_mov_b32_e32 v29, 0
	s_and_saveexec_b64 s[16:17], s[8:9]
	s_cbranch_execz .LBB0_374
	v_ashrrev_i32_e32 v171, 31, v170
	v_lshlrev_b64 v[24:25], 12, v[170:171]
	v_lshl_add_u64 v[24:25], v[166:167], 0, v[24:25]
	v_add_co_u32_e32 v24, vcc, 0xffffe000, v24
	s_nop 1
	v_addc_co_u32_e32 v25, vcc, -1, v25, vcc
	global_load_dwordx4 v[26:29], v[24:25], off nt
.LBB0_374:
	s_or_b64 exec, exec, s[16:17]
	v_mov_b32_e32 v23, 0
	v_mov_b32_e32 v24, 0
	v_mov_b32_e32 v25, 0
	s_and_saveexec_b64 s[16:17], s[8:9]
	s_cbranch_execz .LBB0_376
	v_ashrrev_i32_e32 v171, 31, v170
	v_lshlrev_b64 v[22:23], 12, v[170:171]
	v_lshl_add_u64 v[22:23], v[166:167], 0, v[22:23]
	global_load_dwordx4 v[22:25], v[22:23], off offset:-4096 nt

.LBB0_378:
	s_or_b64 exec, exec, s[16:17]
	v_ashrrev_i32_e32 v171, 31, v170
	s_waitcnt lgkmcnt(7)
	v_lshlrev_b64 v[6:7], 12, v[170:171]
	s_waitcnt lgkmcnt(1)
	v_lshl_add_u64 v[36:37], v[166:167], 0, v[6:7]
	v_or_b32_e32 v6, 1, v170
	v_ashrrev_i32_e32 v7, 31, v6
	s_waitcnt lgkmcnt(0)
	v_lshlrev_b64 v[38:39], 12, v[6:7]
	v_or_b32_e32 v6, 2, v170
	v_ashrrev_i32_e32 v7, 31, v6
	v_lshlrev_b64 v[6:7], 12, v[6:7]
	v_lshl_add_u64 v[40:41], v[166:167], 0, v[6:7]
	v_or_b32_e32 v6, 3, v170
	v_ashrrev_i32_e32 v7, 31, v6
	v_lshlrev_b64 v[6:7], 12, v[6:7]
	v_lshl_add_u64 v[42:43], v[166:167], 0, v[6:7]
	v_or_b32_e32 v6, 4, v170
	v_ashrrev_i32_e32 v7, 31, v6
	v_lshlrev_b64 v[6:7], 12, v[6:7]
	v_lshl_add_u64 v[44:45], v[166:167], 0, v[6:7]
	v_or_b32_e32 v6, 5, v170
	v_ashrrev_i32_e32 v7, 31, v6
	v_lshlrev_b64 v[6:7], 12, v[6:7]
	v_lshl_add_u64 v[46:47], v[166:167], 0, v[6:7]
	v_or_b32_e32 v6, 6, v170
	v_ashrrev_i32_e32 v7, 31, v6
	v_lshlrev_b64 v[6:7], 12, v[6:7]
	v_lshl_add_u64 v[48:49], v[166:167], 0, v[6:7]
	v_or_b32_e32 v6, 7, v170
	v_ashrrev_i32_e32 v7, 31, v6
	v_lshlrev_b64 v[6:7], 12, v[6:7]
	v_lshl_add_u64 v[62:63], v[166:167], 0, v[6:7]
	v_lshl_add_u64 v[38:39], v[166:167], 0, v[38:39]
	s_barrier
	global_load_dwordx4 v[10:13], v[48:49], off nt
	global_load_dwordx4 v[6:9], v[62:63], off nt
	global_load_dwordx4 v[50:53], v[44:45], off nt
	global_load_dwordx4 v[30:33], v[46:47], off nt
	global_load_dwordx4 v[58:61], v[40:41], off nt
	global_load_dwordx4 v[54:57], v[42:43], off nt
	s_nop 0
	global_load_dwordx4 v[62:65], v[38:39], off nt
	global_load_dwordx4 v[66:69], v[36:37], off nt
	ds_read_b128 v[36:39], v34 offset:64
	ds_read_b128 v[40:43], v34 offset:80
	ds_read_b128 v[44:47], v34 offset:96
	ds_read_b128 v[70:73], v34 offset:112
	s_mov_b32 s1, 0
	s_waitcnt lgkmcnt(3)
	v_mov_b32_e32 v34, v37
	v_mov_b32_e32 v35, v38
	v_mov_b32_e32 v37, v39
	v_pk_add_f32 v[34:35], v[34:35], v[36:37]
	s_waitcnt lgkmcnt(2)
	v_mov_b32_e32 v36, v41
	v_mov_b32_e32 v37, v42
	v_mov_b32_e32 v41, v43
	v_pk_add_f32 v[36:37], v[36:37], v[40:41]
	v_add_f32_e32 v34, v34, v35
	v_add_f32_e32 v35, v36, v37
	s_waitcnt lgkmcnt(1)
	v_mov_b32_e32 v38, v45
	v_mov_b32_e32 v39, v46
	v_mov_b32_e32 v45, v47
	v_fmamk_f32 v35, v35, 0x3a800000, v187
	v_pk_add_f32 v[38:39], v[38:39], v[44:45]
	v_fmamk_f32 v34, v34, 0x3a800000, v187
	v_rsq_f32_e32 v36, v35
	v_add_f32_e32 v35, v38, v39
	s_waitcnt lgkmcnt(0)
	v_mov_b32_e32 v40, v71
	v_mov_b32_e32 v41, v72
	v_mov_b32_e32 v71, v73
	v_rsq_f32_e32 v34, v34
	v_fmamk_f32 v35, v35, 0x3a800000, v187
	v_pk_add_f32 v[40:41], v[40:41], v[70:71]
	v_rsq_f32_e32 v38, v35
	v_add_f32_e32 v35, v40, v41
	v_fmamk_f32 v35, v35, 0x3a800000, v187
	v_rsq_f32_e32 v40, v35
	v_pk_mul_f32 v[18:19], v[18:19], v[34:35] op_sel_hi:[1,0]
	v_pk_mul_f32 v[20:21], v[20:21], v[34:35] op_sel_hi:[1,0]
	v_pk_mul_f32 v[86:87], v[2:3], v[18:19]
	v_pk_mul_f32 v[84:85], v[4:5], v[20:21]
	v_pk_mul_f32 v[14:15], v[14:15], v[36:37] op_sel_hi:[1,0]
	v_pk_mul_f32 v[16:17], v[16:17], v[36:37] op_sel_hi:[1,0]
	v_pk_fma_f32 v[18:19], v[2:3], v[18:19], 0 op_sel_hi:[1,1,0]
	v_pk_fma_f32 v[20:21], v[4:5], v[20:21], 0 op_sel_hi:[1,1,0]
	v_pk_mul_f32 v[80:81], v[4:5], v[16:17]
	v_pk_mul_f32 v[82:83], v[2:3], v[14:15]
	v_pk_mul_f32 v[26:27], v[26:27], v[38:39] op_sel_hi:[1,0]
	v_pk_mul_f32 v[28:29], v[28:29], v[38:39] op_sel_hi:[1,0]
	v_pk_fma_f32 v[16:17], v[4:5], v[16:17], v[20:21]
	v_pk_fma_f32 v[14:15], v[2:3], v[14:15], v[18:19]
	v_pk_mul_f32 v[22:23], v[22:23], v[40:41] op_sel_hi:[1,0]
	v_pk_mul_f32 v[24:25], v[24:25], v[40:41] op_sel_hi:[1,0]
	v_pk_fma_f32 v[14:15], v[2:3], v[26:27], v[14:15]
	v_pk_fma_f32 v[16:17], v[4:5], v[28:29], v[16:17]
	v_pk_mul_f32 v[76:77], v[4:5], v[28:29]
	v_pk_mul_f32 v[78:79], v[2:3], v[26:27]
	v_pk_mul_f32 v[72:73], v[4:5], v[24:25]
	v_pk_mul_f32 v[74:75], v[2:3], v[22:23]
	v_pk_fma_f32 v[88:89], v[4:5], v[24:25], v[16:17]
	v_pk_fma_f32 v[90:91], v[2:3], v[22:23], v[14:15]
	s_mov_b32 s0, s23
	s_waitcnt vmcnt(7)
	v_mov_b64_e32 v[48:49], v[12:13]
	s_waitcnt vmcnt(6)
	v_mov_b64_e32 v[44:45], v[8:9]
	s_waitcnt vmcnt(5)
	v_mov_b64_e32 v[38:39], v[50:51]
	s_waitcnt vmcnt(4)
	v_mov_b64_e32 v[36:37], v[32:33]
	s_waitcnt vmcnt(3)
	v_mov_b64_e32 v[26:27], v[58:59]
	s_waitcnt vmcnt(2)
	v_mov_b64_e32 v[22:23], v[54:55]
	s_waitcnt vmcnt(1)
	v_mov_b64_e32 v[14:15], v[62:63]
	s_waitcnt vmcnt(0)
	v_mov_b64_e32 v[18:19], v[66:67]
	v_mov_b64_e32 v[42:43], v[6:7]
	v_mov_b64_e32 v[46:47], v[10:11]
	v_mov_b64_e32 v[34:35], v[30:31]
	v_mov_b64_e32 v[40:41], v[52:53]
	v_mov_b64_e32 v[24:25], v[56:57]
	v_mov_b64_e32 v[28:29], v[60:61]
	v_mov_b64_e32 v[16:17], v[64:65]
	v_mov_b64_e32 v[20:21], v[68:69]
	s_cmp_eq_u32 s1, 56
	v_add_u32_e32 v70, s1, v186
	s_cbranch_scc1 .LBB0_381
	s_branch .LBB0_380

.LBB0_380:
	v_add_u32_e32 v14, 8, v70
	v_ashrrev_i32_e32 v15, 31, v14
	v_lshlrev_b64 v[14:15], 12, v[14:15]
	v_lshl_add_u64 v[22:23], v[166:167], 0, v[14:15]
	v_add_u32_e32 v14, 9, v70
	v_ashrrev_i32_e32 v15, 31, v14
	v_lshlrev_b64 v[14:15], 12, v[14:15]
	v_lshl_add_u64 v[24:25], v[166:167], 0, v[14:15]
	global_load_dwordx4 v[18:21], v[22:23], off nt
	global_load_dwordx4 v[14:17], v[24:25], off nt
	v_add_u32_e32 v22, 10, v70
	v_ashrrev_i32_e32 v23, 31, v22
	v_lshlrev_b64 v[22:23], 12, v[22:23]
	v_lshl_add_u64 v[34:35], v[166:167], 0, v[22:23]
	v_add_u32_e32 v22, 11, v70
	v_ashrrev_i32_e32 v23, 31, v22
	v_lshlrev_b64 v[22:23], 12, v[22:23]
	v_lshl_add_u64 v[36:37], v[166:167], 0, v[22:23]
	global_load_dwordx4 v[26:29], v[34:35], off nt
	global_load_dwordx4 v[22:25], v[36:37], off nt
	v_add_u32_e32 v34, 12, v70
	v_ashrrev_i32_e32 v35, 31, v34
	v_lshlrev_b64 v[34:35], 12, v[34:35]
	v_lshl_add_u64 v[42:43], v[166:167], 0, v[34:35]
	v_add_u32_e32 v34, 13, v70
	v_ashrrev_i32_e32 v35, 31, v34
	v_lshlrev_b64 v[34:35], 12, v[34:35]
	v_lshl_add_u64 v[44:45], v[166:167], 0, v[34:35]
	global_load_dwordx4 v[38:41], v[42:43], off nt
	global_load_dwordx4 v[34:37], v[44:45], off nt
	v_add_u32_e32 v42, 14, v70
	v_ashrrev_i32_e32 v43, 31, v42
	v_lshlrev_b64 v[42:43], 12, v[42:43]
	v_lshl_add_u64 v[92:93], v[166:167], 0, v[42:43]
	v_add_u32_e32 v42, 15, v70
	v_ashrrev_i32_e32 v43, 31, v42
	v_lshlrev_b64 v[42:43], 12, v[42:43]
	v_lshl_add_u64 v[94:95], v[166:167], 0, v[42:43]
	global_load_dwordx4 v[46:49], v[92:93], off nt
	global_load_dwordx4 v[42:45], v[94:95], off nt

.LBB0_385:
	s_and_b64 vcc, exec, s[16:17]
	s_cbranch_vccz .LBB0_247
	v_mov_b32_e32 v6, 0
	v_ashrrev_i32_e32 v171, 31, v170
	s_waitcnt vmcnt(14)
	v_mov_b32_e32 v10, 0
	v_mov_b32_e32 v11, 0
	v_mov_b32_e32 v12, 0
	v_mov_b32_e32 v13, 0
	s_and_saveexec_b64 s[16:17], s[8:9]
	s_cbranch_execz .LBB0_388
	v_lshlrev_b64 v[8:9], 12, v[170:171]
	v_lshl_add_u64 v[8:9], v[166:167], 0, v[8:9]
	v_add_co_u32_e32 v8, vcc, 0xffff0000, v8
	s_nop 1
	v_addc_co_u32_e32 v9, vcc, -1, v9, vcc
	global_load_dwordx4 v[10:13], v[8:9], off nt
.LBB0_388:
	s_or_b64 exec, exec, s[16:17]
	v_mov_b32_e32 v7, 0
	v_mov_b32_e32 v8, 0
	v_mov_b32_e32 v9, 0
	s_and_saveexec_b64 s[16:17], s[8:9]
	s_cbranch_execz .LBB0_390
	v_lshlrev_b64 v[6:7], 12, v[170:171]
	v_lshl_add_u64 v[6:7], v[166:167], 0, v[6:7]
	v_add_co_u32_e32 v6, vcc, 0xffff1000, v6
	s_nop 1
	v_addc_co_u32_e32 v7, vcc, -1, v7, vcc
	global_load_dwordx4 v[6:9], v[6:7], off nt
.LBB0_390:
	s_or_b64 exec, exec, s[16:17]
	v_mov_b32_e32 v14, 0
	s_waitcnt vmcnt(12)
	v_mov_b32_e32 v22, 0
	v_mov_b32_e32 v23, 0
	v_mov_b32_e32 v24, 0
	v_mov_b32_e32 v25, 0
	s_and_saveexec_b64 s[16:17], s[8:9]
	s_cbranch_execz .LBB0_392
	v_lshlrev_b64 v[16:17], 12, v[170:171]
	v_lshl_add_u64 v[16:17], v[166:167], 0, v[16:17]
	v_add_co_u32_e32 v16, vcc, 0xffff2000, v16
	s_nop 1
	v_addc_co_u32_e32 v17, vcc, -1, v17, vcc
	global_load_dwordx4 v[22:25], v[16:17], off nt
.LBB0_392:
	s_or_b64 exec, exec, s[16:17]
	v_mov_b32_e32 v15, 0
	v_mov_b32_e32 v16, 0
	v_mov_b32_e32 v17, 0
	s_and_saveexec_b64 s[16:17], s[8:9]
	s_cbranch_execz .LBB0_394
	v_lshlrev_b64 v[14:15], 12, v[170:171]
	v_lshl_add_u64 v[14:15], v[166:167], 0, v[14:15]
	v_add_co_u32_e32 v14, vcc, 0xffff3000, v14
	s_nop 1
	v_addc_co_u32_e32 v15, vcc, -1, v15, vcc
	global_load_dwordx4 v[14:17], v[14:15], off nt
.LBB0_394:
	s_or_b64 exec, exec, s[16:17]
	v_mov_b32_e32 v18, 0
	s_waitcnt vmcnt(10)
	v_mov_b32_e32 v30, 0
	v_mov_b32_e32 v31, 0
	v_mov_b32_e32 v32, 0
	v_mov_b32_e32 v33, 0
	s_and_saveexec_b64 s[16:17], s[8:9]
	s_cbranch_execz .LBB0_396
	v_lshlrev_b64 v[20:21], 12, v[170:171]
	v_lshl_add_u64 v[20:21], v[166:167], 0, v[20:21]
	v_add_co_u32_e32 v20, vcc, 0xffff4000, v20
	s_nop 1
	v_addc_co_u32_e32 v21, vcc, -1, v21, vcc
	global_load_dwordx4 v[30:33], v[20:21], off nt
.LBB0_396:
	s_or_b64 exec, exec, s[16:17]
	v_mov_b32_e32 v19, 0
	v_mov_b32_e32 v20, 0
	v_mov_b32_e32 v21, 0
	s_and_saveexec_b64 s[16:17], s[8:9]
	s_cbranch_execz .LBB0_398
	v_lshlrev_b64 v[18:19], 12, v[170:171]
	v_lshl_add_u64 v[18:19], v[166:167], 0, v[18:19]
	v_add_co_u32_e32 v18, vcc, 0xffff5000, v18
	s_nop 1
	v_addc_co_u32_e32 v19, vcc, -1, v19, vcc
	global_load_dwordx4 v[18:21], v[18:19], off nt
.LBB0_398:
	s_or_b64 exec, exec, s[16:17]
	v_mov_b32_e32 v26, 0
	s_waitcnt vmcnt(10)
	v_mov_b32_e32 v34, 0
	v_mov_b32_e32 v35, 0
	v_mov_b32_e32 v36, 0
	v_mov_b32_e32 v37, 0
	s_and_saveexec_b64 s[16:17], s[8:9]
	s_cbranch_execz .LBB0_400
	v_lshlrev_b64 v[28:29], 12, v[170:171]
	v_lshl_add_u64 v[28:29], v[166:167], 0, v[28:29]
	v_add_co_u32_e32 v28, vcc, 0xffff6000, v28
	s_nop 1
	v_addc_co_u32_e32 v29, vcc, -1, v29, vcc
	global_load_dwordx4 v[34:37], v[28:29], off nt
.LBB0_400:
	s_or_b64 exec, exec, s[16:17]
	v_mov_b32_e32 v27, 0
	v_mov_b32_e32 v28, 0
	v_mov_b32_e32 v29, 0
	s_and_saveexec_b64 s[16:17], s[8:9]
	s_cbranch_execz .LBB0_402
	v_lshlrev_b64 v[26:27], 12, v[170:171]
	v_lshl_add_u64 v[26:27], v[166:167], 0, v[26:27]
	v_add_co_u32_e32 v26, vcc, 0xffff7000, v26
	s_nop 1
	v_addc_co_u32_e32 v27, vcc, -1, v27, vcc
	global_load_dwordx4 v[26:29], v[26:27], off nt

.LBB0_404:
	s_or_b64 exec, exec, s[16:17]
	v_mov_b32_e32 v6, 0
	v_mov_b32_e32 v10, 0
	s_waitcnt lgkmcnt(5)
	v_mov_b32_e32 v11, 0
	v_mov_b32_e32 v12, 0
	s_waitcnt lgkmcnt(4)
	v_mov_b32_e32 v13, 0
	s_waitcnt lgkmcnt(0)
	s_barrier
	s_and_saveexec_b64 s[16:17], s[8:9]
	s_cbranch_execz .LBB0_406
	v_lshlrev_b64 v[8:9], 12, v[170:171]
	v_lshl_add_u64 v[8:9], v[166:167], 0, v[8:9]
	v_add_co_u32_e32 v8, vcc, 0xffff8000, v8
	s_nop 1
	v_addc_co_u32_e32 v9, vcc, -1, v9, vcc
	global_load_dwordx4 v[10:13], v[8:9], off nt
.LBB0_406:
	s_or_b64 exec, exec, s[16:17]
	v_mov_b32_e32 v7, 0
	v_mov_b32_e32 v8, 0
	v_mov_b32_e32 v9, 0
	s_and_saveexec_b64 s[16:17], s[8:9]
	s_cbranch_execz .LBB0_408
	v_lshlrev_b64 v[6:7], 12, v[170:171]
	v_lshl_add_u64 v[6:7], v[166:167], 0, v[6:7]
	v_add_co_u32_e32 v6, vcc, 0xffff9000, v6
	s_nop 1
	v_addc_co_u32_e32 v7, vcc, -1, v7, vcc
	global_load_dwordx4 v[6:9], v[6:7], off nt
.LBB0_408:
	s_or_b64 exec, exec, s[16:17]
	v_mov_b32_e32 v22, 0
	v_mov_b32_e32 v30, 0
	v_mov_b32_e32 v31, 0
	v_mov_b32_e32 v32, 0
	v_mov_b32_e32 v33, 0
	s_and_saveexec_b64 s[16:17], s[8:9]
	s_cbranch_execz .LBB0_410
	v_lshlrev_b64 v[14:15], 12, v[170:171]
	v_lshl_add_u64 v[14:15], v[166:167], 0, v[14:15]
	v_add_co_u32_e32 v14, vcc, 0xffffa000, v14
	s_nop 1
	v_addc_co_u32_e32 v15, vcc, -1, v15, vcc
	global_load_dwordx4 v[30:33], v[14:15], off nt
.LBB0_410:
	s_or_b64 exec, exec, s[16:17]
	v_mov_b32_e32 v23, 0
	v_mov_b32_e32 v24, 0
	v_mov_b32_e32 v25, 0
	s_and_saveexec_b64 s[16:17], s[8:9]
	s_cbranch_execz .LBB0_412
	v_lshlrev_b64 v[14:15], 12, v[170:171]
	v_lshl_add_u64 v[14:15], v[166:167], 0, v[14:15]
	v_add_co_u32_e32 v14, vcc, 0xffffb000, v14
	s_nop 1
	v_addc_co_u32_e32 v15, vcc, -1, v15, vcc
	global_load_dwordx4 v[22:25], v[14:15], off nt
.LBB0_412:
	s_or_b64 exec, exec, s[16:17]
	v_mov_b32_e32 v26, 0
	v_mov_b32_e32 v34, 0
	v_mov_b32_e32 v35, 0
	v_mov_b32_e32 v36, 0
	v_mov_b32_e32 v37, 0
	s_and_saveexec_b64 s[16:17], s[8:9]
	s_cbranch_execz .LBB0_414
	v_lshlrev_b64 v[14:15], 12, v[170:171]
	v_lshl_add_u64 v[14:15], v[166:167], 0, v[14:15]
	v_add_co_u32_e32 v14, vcc, 0xffffc000, v14
	s_nop 1
	v_addc_co_u32_e32 v15, vcc, -1, v15, vcc
	global_load_dwordx4 v[34:37], v[14:15], off nt
.LBB0_414:
	s_or_b64 exec, exec, s[16:17]
	v_mov_b32_e32 v27, 0
	v_mov_b32_e32 v28, 0
	v_mov_b32_e32 v29, 0
	s_and_saveexec_b64 s[16:17], s[8:9]
	s_cbranch_execz .LBB0_416
	v_lshlrev_b64 v[14:15], 12, v[170:171]
	v_lshl_add_u64 v[14:15], v[166:167], 0, v[14:15]
	v_add_co_u32_e32 v14, vcc, 0xffffd000, v14
	s_nop 1
	v_addc_co_u32_e32 v15, vcc, -1, v15, vcc
	global_load_dwordx4 v[26:29], v[14:15], off nt
.LBB0_416:
	s_or_b64 exec, exec, s[16:17]
	v_mov_b32_e32 v14, 0
	v_mov_b32_e32 v18, 0
	v_mov_b32_e32 v19, 0
	v_mov_b32_e32 v20, 0
	v_mov_b32_e32 v21, 0
	s_and_saveexec_b64 s[16:17], s[8:9]
	s_cbranch_execz .LBB0_418
	v_lshlrev_b64 v[16:17], 12, v[170:171]
	v_lshl_add_u64 v[16:17], v[166:167], 0, v[16:17]
	v_add_co_u32_e32 v16, vcc, 0xffffe000, v16
	s_nop 1
	v_addc_co_u32_e32 v17, vcc, -1, v17, vcc
	global_load_dwordx4 v[18:21], v[16:17], off nt
.LBB0_418:
	s_or_b64 exec, exec, s[16:17]
	v_mov_b32_e32 v15, 0
	v_mov_b32_e32 v16, 0
	v_mov_b32_e32 v17, 0
	s_and_saveexec_b64 s[16:17], s[8:9]
	s_cbranch_execz .LBB0_420
	v_lshlrev_b64 v[14:15], 12, v[170:171]
	v_lshl_add_u64 v[14:15], v[166:167], 0, v[14:15]
	global_load_dwordx4 v[14:17], v[14:15], off offset:-4096 nt

.LBB0_422:
	s_or_b64 exec, exec, s[8:9]
	s_waitcnt lgkmcnt(7)
	v_lshlrev_b64 v[6:7], 12, v[170:171]
	s_waitcnt lgkmcnt(3)
	v_lshl_add_u64 v[24:25], v[166:167], 0, v[6:7]
	v_or_b32_e32 v6, 1, v170
	v_ashrrev_i32_e32 v7, 31, v6
	s_waitcnt lgkmcnt(2)
	v_lshlrev_b64 v[26:27], 12, v[6:7]
	v_or_b32_e32 v6, 2, v170
	v_ashrrev_i32_e32 v7, 31, v6
	v_lshlrev_b64 v[6:7], 12, v[6:7]
	s_waitcnt lgkmcnt(1)
	v_lshl_add_u64 v[28:29], v[166:167], 0, v[6:7]
	v_or_b32_e32 v6, 3, v170
	v_ashrrev_i32_e32 v7, 31, v6
	v_lshlrev_b64 v[6:7], 12, v[6:7]
	s_waitcnt lgkmcnt(0)
	v_lshl_add_u64 v[30:31], v[166:167], 0, v[6:7]
	v_or_b32_e32 v6, 4, v170
	v_ashrrev_i32_e32 v7, 31, v6
	v_lshlrev_b64 v[6:7], 12, v[6:7]
	v_lshl_add_u64 v[32:33], v[166:167], 0, v[6:7]
	v_or_b32_e32 v6, 5, v170
	v_ashrrev_i32_e32 v7, 31, v6
	v_lshlrev_b64 v[6:7], 12, v[6:7]
	v_lshl_add_u64 v[34:35], v[166:167], 0, v[6:7]
	v_or_b32_e32 v6, 6, v170
	v_ashrrev_i32_e32 v7, 31, v6
	v_lshlrev_b64 v[6:7], 12, v[6:7]
	v_lshl_add_u64 v[36:37], v[166:167], 0, v[6:7]
	v_or_b32_e32 v6, 7, v170
	v_ashrrev_i32_e32 v7, 31, v6
	v_lshlrev_b64 v[6:7], 12, v[6:7]
	v_lshl_add_u64 v[26:27], v[166:167], 0, v[26:27]
	s_barrier
	v_lshl_add_u64 v[42:43], v[166:167], 0, v[6:7]
	global_load_dwordx4 v[10:13], v[36:37], off nt
	global_load_dwordx4 v[6:9], v[42:43], off nt
	global_load_dwordx4 v[50:53], v[32:33], off nt
	global_load_dwordx4 v[38:41], v[34:35], off nt
	global_load_dwordx4 v[58:61], v[28:29], off nt
	global_load_dwordx4 v[54:57], v[30:31], off nt
	global_load_dwordx4 v[62:65], v[26:27], off nt
	global_load_dwordx4 v[66:69], v[24:25], off nt
	ds_read_b128 v[24:27], v22 offset:96
	ds_read_b128 v[28:31], v22 offset:112
	s_mov_b32 s0, 0
	s_mov_b32 s1, 0
	s_waitcnt lgkmcnt(1)
	v_mov_b32_e32 v22, v25
	v_mov_b32_e32 v23, v26
	v_mov_b32_e32 v25, v27
	s_waitcnt lgkmcnt(0)
	v_mov_b32_e32 v26, v29
	v_mov_b32_e32 v27, v30
	v_mov_b32_e32 v29, v31
	v_pk_add_f32 v[22:23], v[22:23], v[24:25]
	v_pk_add_f32 v[24:25], v[26:27], v[28:29]
	v_add_f32_e32 v22, v22, v23
	v_add_f32_e32 v23, v24, v25
	v_fmamk_f32 v22, v22, 0x3a800000, v187
	v_rsq_f32_e32 v22, v22
	v_fmamk_f32 v23, v23, 0x3a800000, v187
	v_rsq_f32_e32 v24, v23
	v_pk_mul_f32 v[18:19], v[18:19], v[22:23] op_sel_hi:[1,0]
	v_pk_mul_f32 v[20:21], v[20:21], v[22:23] op_sel_hi:[1,0]
	v_pk_mul_f32 v[14:15], v[14:15], v[24:25] op_sel_hi:[1,0]
	v_pk_mul_f32 v[16:17], v[16:17], v[24:25] op_sel_hi:[1,0]
	v_pk_mul_f32 v[76:77], v[4:5], v[20:21]
	v_pk_mul_f32 v[78:79], v[2:3], v[18:19]
	v_pk_fma_f32 v[18:19], v[2:3], v[18:19], 0 op_sel_hi:[1,1,0]
	v_pk_fma_f32 v[20:21], v[4:5], v[20:21], 0 op_sel_hi:[1,1,0]
	v_pk_mul_f32 v[72:73], v[4:5], v[16:17]
	v_pk_mul_f32 v[74:75], v[2:3], v[14:15]
	v_pk_fma_f32 v[80:81], v[4:5], v[16:17], v[20:21]
	v_pk_fma_f32 v[82:83], v[2:3], v[14:15], v[18:19]
	s_waitcnt vmcnt(7)
	v_mov_b64_e32 v[48:49], v[12:13]
	s_waitcnt vmcnt(6)
	v_mov_b64_e32 v[44:45], v[8:9]
	s_waitcnt vmcnt(5)
	v_mov_b64_e32 v[34:35], v[50:51]
	s_waitcnt vmcnt(4)
	v_mov_b64_e32 v[30:31], v[38:39]
	s_waitcnt vmcnt(3)
	v_mov_b64_e32 v[26:27], v[58:59]
	s_waitcnt vmcnt(2)
	v_mov_b64_e32 v[22:23], v[54:55]
	s_waitcnt vmcnt(1)
	v_mov_b64_e32 v[14:15], v[62:63]
	s_waitcnt vmcnt(0)
	v_mov_b64_e32 v[18:19], v[66:67]
	v_mov_b64_e32 v[42:43], v[6:7]
	v_mov_b64_e32 v[46:47], v[10:11]
	v_mov_b64_e32 v[32:33], v[40:41]
	v_mov_b64_e32 v[36:37], v[52:53]
	v_mov_b64_e32 v[24:25], v[56:57]
	v_mov_b64_e32 v[28:29], v[60:61]
	v_mov_b64_e32 v[16:17], v[64:65]
	v_mov_b64_e32 v[20:21], v[68:69]
	s_cmp_eq_u32 s0, 56
	v_add_u32_e32 v70, s0, v186
	s_cbranch_scc1 .LBB0_425
	s_branch .LBB0_424

.LBB0_424:
	v_add_u32_e32 v14, 8, v70
	v_ashrrev_i32_e32 v15, 31, v14
	v_lshlrev_b64 v[14:15], 12, v[14:15]
	v_lshl_add_u64 v[22:23], v[166:167], 0, v[14:15]
	v_add_u32_e32 v14, 9, v70
	v_ashrrev_i32_e32 v15, 31, v14
	v_lshlrev_b64 v[14:15], 12, v[14:15]
	v_lshl_add_u64 v[24:25], v[166:167], 0, v[14:15]
	global_load_dwordx4 v[18:21], v[22:23], off nt
	global_load_dwordx4 v[14:17], v[24:25], off nt
	v_add_u32_e32 v22, 10, v70
	v_ashrrev_i32_e32 v23, 31, v22
	v_lshlrev_b64 v[22:23], 12, v[22:23]
	v_lshl_add_u64 v[30:31], v[166:167], 0, v[22:23]
	v_add_u32_e32 v22, 11, v70
	v_ashrrev_i32_e32 v23, 31, v22
	v_lshlrev_b64 v[22:23], 12, v[22:23]
	v_lshl_add_u64 v[32:33], v[166:167], 0, v[22:23]
	global_load_dwordx4 v[26:29], v[30:31], off nt
	global_load_dwordx4 v[22:25], v[32:33], off nt
	v_add_u32_e32 v30, 12, v70
	v_ashrrev_i32_e32 v31, 31, v30
	v_lshlrev_b64 v[30:31], 12, v[30:31]
	v_lshl_add_u64 v[42:43], v[166:167], 0, v[30:31]
	v_add_u32_e32 v30, 13, v70
	v_ashrrev_i32_e32 v31, 31, v30
	v_lshlrev_b64 v[30:31], 12, v[30:31]
	v_lshl_add_u64 v[44:45], v[166:167], 0, v[30:31]
	global_load_dwordx4 v[34:37], v[42:43], off nt
	global_load_dwordx4 v[30:33], v[44:45], off nt
	v_add_u32_e32 v42, 14, v70
	v_ashrrev_i32_e32 v43, 31, v42
	v_lshlrev_b64 v[42:43], 12, v[42:43]
	v_lshl_add_u64 v[84:85], v[166:167], 0, v[42:43]
	v_add_u32_e32 v42, 15, v70
	v_ashrrev_i32_e32 v43, 31, v42
	v_lshlrev_b64 v[42:43], 12, v[42:43]
	v_lshl_add_u64 v[86:87], v[166:167], 0, v[42:43]
	global_load_dwordx4 v[46:49], v[84:85], off nt
	global_load_dwordx4 v[42:45], v[86:87], off nt
